# speedup vs baseline: 1.0129x; 1.0008x over previous
_Z8k_stageAPKfS0_S0_S0_PDF16_PKDF16_S0_S1_ii:
	s_load_dwordx2 s[86:87], s[0:1], 0x28
	s_load_dwordx2 s[82:83], s[0:1], 0x40
	s_mov_b32 s81, s3
	s_load_dwordx2 s[64:65], s[0:1], 0x40
	v_readfirstlane_b32 s94, v0
	s_nop 0
	s_lshr_b32 s94, s94, 6
	s_load_dwordx8 s[4:11], s[0:1], 0x0
	v_readfirstlane_b32 s14, v0
	s_lshr_b32 s15, s2, 5
	s_lshl_b32 s2, s2, 7
	s_lshr_b32 s20, s14, 6
	s_and_b32 s12, s2, 0xf80
	s_lshl_b32 s13, s15, 12
	s_mov_b32 s18, s3
	s_cmpk_lt_u32 s14, 0x100
	s_waitcnt lgkmcnt(0)
	s_cselect_b32 s2, s4, s6
	s_cselect_b32 s3, s5, s7
	s_cselect_b32 s4, s8, s10
	s_cselect_b32 s5, s9, s11
	s_cmp_eq_u32 s18, 0
	s_cselect_b32 s3, s3, s5
	s_cselect_b32 s2, s2, s4
	s_lshr_b32 s5, s14, 1
	s_lshl_b32 s4, s15, 7
	s_and_b32 s5, s5, 0x60
	v_bfe_u32 v1, v0, 5, 1
	s_or_b32 s4, s5, s4
	v_lshl_or_b32 v82, v1, 3, s4
	v_mov_b32_e32 v83, 0
	v_lshlrev_b64 v[2:3], 14, v[82:83]
	v_lshlrev_b32_e32 v78, 2, v0
	s_mov_b32 s17, 0
	v_lshl_add_u64 v[2:3], s[2:3], 0, v[2:3]
	s_lshl_b32 s16, s12, 2
	v_and_b32_e32 v79, 0x7c, v78
	v_lshl_add_u64 v[2:3], v[2:3], 0, s[16:17]
	v_lshlrev_b32_e32 v82, 2, v79
	v_lshl_add_u64 v[42:43], v[2:3], 0, v[82:83]
	s_movk_i32 s21, 0x4000
	v_add_co_u32_e32 v10, vcc, s21, v42
	s_mov_b32 s2, 0x8000
	s_nop 0
	v_addc_co_u32_e32 v11, vcc, 0, v43, vcc
	v_add_co_u32_e32 v18, vcc, s2, v42
	s_mov_b32 s2, 0xc000
	s_nop 0
	v_addc_co_u32_e32 v19, vcc, 0, v43, vcc
	v_add_co_u32_e32 v20, vcc, s2, v42
	s_mov_b32 s14, 0x10000
	s_nop 0
	v_addc_co_u32_e32 v21, vcc, 0, v43, vcc
	v_add_co_u32_e32 v26, vcc, s14, v42
	s_mov_b32 s2, 0x14000
	s_nop 0
	v_addc_co_u32_e32 v27, vcc, 0, v43, vcc
	v_add_co_u32_e32 v28, vcc, s2, v42
	s_mov_b32 s2, 0x18000
	s_nop 0
	v_addc_co_u32_e32 v29, vcc, 0, v43, vcc
	v_add_co_u32_e32 v34, vcc, s2, v42
	s_mov_b32 s2, 0x1c000
	s_nop 0
	v_addc_co_u32_e32 v35, vcc, 0, v43, vcc
	v_add_co_u32_e32 v36, vcc, s2, v42
	s_mov_b32 s2, 0x40000
	s_nop 0
	v_addc_co_u32_e32 v37, vcc, 0, v43, vcc
	v_add_co_u32_e32 v66, vcc, s2, v42
	s_mov_b32 s2, 0x44000
	s_nop 0
	v_addc_co_u32_e32 v67, vcc, 0, v43, vcc
	v_add_co_u32_e32 v68, vcc, s2, v42
	s_mov_b32 s2, 0x48000
	s_nop 0
	v_addc_co_u32_e32 v69, vcc, 0, v43, vcc
	global_load_dwordx4 v[2:5], v[42:43], off nt
	global_load_dwordx4 v[6:9], v[10:11], off nt
	v_add_co_u32_e32 v44, vcc, s2, v42
	global_load_dwordx4 v[10:13], v[18:19], off nt
	global_load_dwordx4 v[14:17], v[20:21], off nt
	s_nop 0
	global_load_dwordx4 v[18:21], v[26:27], off nt
	global_load_dwordx4 v[22:25], v[28:29], off nt
	s_nop 0
	global_load_dwordx4 v[26:29], v[34:35], off nt
	global_load_dwordx4 v[30:33], v[36:37], off nt
	v_addc_co_u32_e32 v45, vcc, 0, v43, vcc
	s_mov_b32 s2, 0x4c000
	v_add_co_u32_e32 v46, vcc, s2, v42
	s_mov_b32 s2, 0x50000
	s_nop 0
	v_addc_co_u32_e32 v47, vcc, 0, v43, vcc
	v_add_co_u32_e32 v70, vcc, s2, v42
	s_mov_b32 s2, 0x54000
	s_nop 0
	v_addc_co_u32_e32 v71, vcc, 0, v43, vcc
	v_add_co_u32_e32 v72, vcc, s2, v42
	s_mov_b32 s2, 0x58000
	s_nop 0
	v_addc_co_u32_e32 v73, vcc, 0, v43, vcc
	v_add_co_u32_e32 v74, vcc, s2, v42
	s_mov_b32 s2, 0x5c000
	s_nop 0
	v_addc_co_u32_e32 v75, vcc, 0, v43, vcc
	v_add_co_u32_e32 v76, vcc, s2, v42
	global_load_dwordx4 v[34:37], v[44:45], off nt
	global_load_dwordx4 v[38:41], v[46:47], off nt
	v_addc_co_u32_e32 v77, vcc, 0, v43, vcc
	global_load_dwordx4 v[42:45], v[74:75], off nt
	global_load_dwordx4 v[46:49], v[76:77], off nt
	global_load_dwordx4 v[50:53], v[70:71], off nt
	global_load_dwordx4 v[54:57], v[72:73], off nt
	global_load_dwordx4 v[58:61], v[66:67], off nt
	global_load_dwordx4 v[62:65], v[68:69], off nt
	v_lshl_or_b32 v1, s20, 2, v1
	v_lshrrev_b32_e32 v70, 5, v0
	v_or_b32_e32 v141, 0x200, v0
	v_or_b32_e32 v142, 0x600, v0
	s_or_b32 s16, s13, s12
	s_ashr_i32 s19, s18, 31
	s_lshl_b64 s[12:13], s[16:17], 9
	s_mov_b32 s15, 0x20000
	v_or_b32_e32 v144, 0xa00, v0
	v_bfe_u32 v140, v0, 4, 2
	v_and_b32_e32 v145, 15, v0
	v_lshlrev_b32_e32 v220, 9, v145
	s_waitcnt vmcnt(14)
	v_cvt_pk_f16_f32 v66, v2, v6
	v_lshlrev_b32_e32 v6, 9, v79
	v_bitop3_b32 v2, v78, v1, 12 bitop3:0x6c
	s_waitcnt vmcnt(12)
	v_cvt_pk_f16_f32 v67, v10, v14
	s_waitcnt vmcnt(10)
	v_cvt_pk_f16_f32 v68, v18, v22
	s_waitcnt vmcnt(8)
	v_cvt_pk_f16_f32 v69, v26, v30
	v_lshl_add_u32 v2, v2, 4, v6
	ds_write_b128 v2, v[66:69]
	v_cvt_pk_f16_f32 v66, v3, v7
	v_or_b32_e32 v7, 1, v79
	v_lshlrev_b32_e32 v10, 9, v7
	v_bitop3_b32 v2, v7, v1, 13 bitop3:0x6c
	v_cvt_pk_f16_f32 v69, v27, v31
	v_cvt_pk_f16_f32 v68, v19, v23
	v_cvt_pk_f16_f32 v67, v11, v15
	v_lshl_add_u32 v2, v2, 4, v10
	ds_write_b128 v2, v[66:69]
	v_cvt_pk_f16_f32 v66, v4, v8
	v_or_b32_e32 v8, 2, v79
	v_lshlrev_b32_e32 v11, 9, v8
	v_bitop3_b32 v2, v8, v1, 14 bitop3:0x6c
	v_cvt_pk_f16_f32 v69, v28, v32
	v_cvt_pk_f16_f32 v68, v20, v24
	v_cvt_pk_f16_f32 v67, v12, v16
	v_lshl_add_u32 v2, v2, 4, v11
	v_cvt_pk_f16_f32 v12, v5, v9
	v_or_b32_e32 v9, 3, v79
	ds_write_b128 v2, v[66:69]
	v_lshlrev_b32_e32 v16, 9, v9
	v_bitop3_b32 v2, v9, v1, 15 bitop3:0x6c
	v_cvt_pk_f16_f32 v15, v29, v33
	v_cvt_pk_f16_f32 v14, v21, v25
	v_cvt_pk_f16_f32 v13, v13, v17
	v_lshl_add_u32 v2, v2, 4, v16
	v_or_b32_e32 v1, 2, v1
	ds_write_b128 v2, v[12:15]
	v_bitop3_b32 v12, v78, v1, 12 bitop3:0x6c
	s_waitcnt vmcnt(4)
	v_cvt_pk_f16_f32 v5, v42, v46
	s_waitcnt vmcnt(2)
	v_cvt_pk_f16_f32 v4, v50, v54
	v_cvt_pk_f16_f32 v3, v34, v38
	s_waitcnt vmcnt(0)
	v_cvt_pk_f16_f32 v2, v58, v62
	v_lshl_add_u32 v6, v12, 4, v6
	ds_write_b128 v6, v[2:5]
	v_bitop3_b32 v6, v7, v1, 13 bitop3:0x6c
	v_cvt_pk_f16_f32 v5, v43, v47
	v_cvt_pk_f16_f32 v4, v51, v55
	v_cvt_pk_f16_f32 v3, v35, v39
	v_cvt_pk_f16_f32 v2, v59, v63
	v_lshl_add_u32 v6, v6, 4, v10
	ds_write_b128 v6, v[2:5]
	v_bitop3_b32 v6, v8, v1, 14 bitop3:0x6c
	v_cvt_pk_f16_f32 v5, v44, v48
	v_cvt_pk_f16_f32 v4, v52, v56
	v_cvt_pk_f16_f32 v3, v36, v40
	v_cvt_pk_f16_f32 v2, v60, v64
	v_lshl_add_u32 v6, v6, 4, v11
	v_bitop3_b32 v1, v9, v1, 15 bitop3:0x6c
	ds_write_b128 v6, v[2:5]
	v_cvt_pk_f16_f32 v5, v45, v49
	v_cvt_pk_f16_f32 v4, v53, v57
	v_cvt_pk_f16_f32 v3, v37, v41
	v_cvt_pk_f16_f32 v2, v61, v65
	v_lshl_add_u32 v1, v1, 4, v16
	ds_write_b128 v1, v[2:5]
	v_bitop3_b32 v2, v70, v0, 31 bitop3:0x78
	v_lshlrev_b32_e32 v1, 9, v70
	v_lshlrev_b32_e32 v22, 4, v2
	v_or_b32_e32 v10, v22, v1
	s_waitcnt lgkmcnt(0)
	s_barrier
	s_mul_i32 s84, s81, s83
	s_add_i32 s84, s84, s82
	s_mul_i32 s84, s84, 0x60000
	s_mul_i32 s85, s94, 0x6000
	s_add_u32 s84, s84, s85
	s_add_u32 s88, s86, s84
	s_addc_u32 s89, s87, 0
	v_mbcnt_lo_u32_b32 v251, -1, 0
	v_mbcnt_hi_u32_b32 v251, -1, v251
	v_lshlrev_b32_e32 v251, 4, v251
	global_load_dwordx4 v[252:255], v251, s[88:89]
	global_load_dwordx4 v[252:255], v251, s[88:89] offset:1024
	global_load_dwordx4 v[252:255], v251, s[88:89] offset:2048
	global_load_dwordx4 v[252:255], v251, s[88:89] offset:3072
	s_add_u32 s88, s88, 0x1000
	s_addc_u32 s89, s89, 0
	global_load_dwordx4 v[252:255], v251, s[88:89]
	global_load_dwordx4 v[252:255], v251, s[88:89] offset:1024
	global_load_dwordx4 v[252:255], v251, s[88:89] offset:2048
	global_load_dwordx4 v[252:255], v251, s[88:89] offset:3072
	s_add_u32 s88, s88, 0x1000
	s_addc_u32 s89, s89, 0
	global_load_dwordx4 v[252:255], v251, s[88:89]
	global_load_dwordx4 v[252:255], v251, s[88:89] offset:1024
	global_load_dwordx4 v[252:255], v251, s[88:89] offset:2048
	global_load_dwordx4 v[252:255], v251, s[88:89] offset:3072
	ds_read_b128 v[2:5], v10
	s_load_dwordx8 s[4:11], s[0:1], 0x20
	s_load_dwordx2 s[2:3], s[0:1], 0x40
	v_lshlrev_b32_e32 v24, 4, v0
	v_and_b32_e32 v25, 0x1e00, v24
	v_or_b32_e32 v26, v22, v25
	s_waitcnt lgkmcnt(0)
	v_pk_max_f16 v6, v5, v5
	v_and_b32_e32 v18, 31, v0
	v_pk_max_f16 v9, v6, 0
	v_pk_max_f16 v6, v4, v4
	v_lshlrev_b32_e32 v29, 4, v18
	v_pk_max_f16 v8, v6, 0
	v_pk_max_f16 v6, v3, v3
	s_lshl_b64 s[0:1], s[18:19], 23
	v_pk_max_f16 v7, v6, 0
	v_pk_max_f16 v6, v2, v2
	s_add_u32 s0, s4, s0
	v_pk_max_f16 v6, v6, 0
	ds_write_b128 v10, v[6:9]
	v_lshlrev_b32_e32 v6, 4, v141
	v_and_b32_e32 v23, 0x3e00, v6
	v_or_b32_e32 v14, v22, v23
	ds_read_b128 v[6:9], v14
	s_addc_u32 s1, s5, s1
	s_add_u32 s12, s0, s12
	s_addc_u32 s0, s1, s13
	s_and_b32 s13, s0, 0xffff
	s_waitcnt lgkmcnt(0)
	v_pk_max_f16 v10, v9, v9
	v_or_b32_e32 v1, v1, v29
	v_pk_max_f16 v13, v10, 0
	v_pk_max_f16 v10, v8, v8
	buffer_store_dwordx4 v[2:5], v1, s[12:15], 0 offen sc1
	v_pk_max_f16 v12, v10, 0
	v_pk_max_f16 v10, v7, v7
	v_or_b32_e32 v1, v23, v29
	v_pk_max_f16 v11, v10, 0
	v_pk_max_f16 v10, v6, v6
	buffer_store_dwordx4 v[6:9], v1, s[12:15], 0 offen sc1
	v_pk_max_f16 v10, v10, 0
	ds_write_b128 v14, v[10:13]
	ds_read_b128 v[10:13], v26 offset:16384
	v_or_b32_e32 v25, v25, v29
	v_or_b32_e32 v6, 0x4000, v25
	s_mov_b32 s0, 0xfe00
	s_waitcnt lgkmcnt(0)
	v_pk_max_f16 v14, v13, v13
	s_nop 0
	v_pk_max_f16 v17, v14, 0
	v_pk_max_f16 v14, v12, v12
	buffer_store_dwordx4 v[10:13], v6, s[12:15], 0 offen sc1
	v_pk_max_f16 v16, v14, 0
	v_pk_max_f16 v14, v11, v11
	s_nop 0
	v_pk_max_f16 v15, v14, 0
	v_pk_max_f16 v14, v10, v10
	s_nop 0
	v_pk_max_f16 v14, v14, 0
	ds_write_b128 v26, v[14:17] offset:16384
	v_lshlrev_b32_e32 v14, 4, v142
	v_and_b32_e32 v27, 0x7e00, v14
	v_or_b32_e32 v28, v22, v27
	ds_read_b128 v[14:17], v28
	v_or_b32_e32 v10, v27, v29
	s_waitcnt lgkmcnt(0)
	v_pk_max_f16 v18, v17, v17
	s_nop 0
	v_pk_max_f16 v21, v18, 0
	v_pk_max_f16 v18, v16, v16
	buffer_store_dwordx4 v[14:17], v10, s[12:15], 0 offen sc1
	v_pk_max_f16 v20, v18, 0
	v_pk_max_f16 v18, v15, v15
	v_or_b32_e32 v10, 0x8000, v25
	v_pk_max_f16 v19, v18, 0
	v_pk_max_f16 v18, v14, v14
	s_nop 0
	v_pk_max_f16 v18, v18, 0
	ds_write_b128 v28, v[18:21]
	ds_read_b128 v[18:21], v26 offset:32768
	s_waitcnt lgkmcnt(0)
	v_pk_max_f16 v1, v21, v21
	s_nop 0
	v_pk_max_f16 v5, v1, 0
	v_pk_max_f16 v1, v20, v20
	buffer_store_dwordx4 v[18:21], v10, s[12:15], 0 offen sc1
	v_pk_max_f16 v4, v1, 0
	v_pk_max_f16 v1, v19, v19
	s_nop 0
	v_pk_max_f16 v3, v1, 0
	v_pk_max_f16 v1, v18, v18
	s_nop 0
	v_pk_max_f16 v2, v1, 0
	v_lshlrev_b32_e32 v1, 4, v144
	v_and_b32_e32 v1, 0xbe00, v1
	ds_write_b128 v26, v[2:5] offset:32768
	v_or_b32_e32 v23, v22, v1
	ds_read_b128 v[2:5], v23
	v_or_b32_e32 v1, v1, v29
	s_waitcnt lgkmcnt(0)
	v_pk_max_f16 v6, v5, v5
	s_nop 0
	v_pk_max_f16 v9, v6, 0
	v_pk_max_f16 v6, v4, v4
	buffer_store_dwordx4 v[2:5], v1, s[12:15], 0 offen sc1
	v_pk_max_f16 v8, v6, 0
	v_pk_max_f16 v6, v3, v3
	v_or_b32_e32 v1, 0xc000, v25
	v_pk_max_f16 v7, v6, 0
	v_pk_max_f16 v6, v2, v2
	s_nop 0
	v_pk_max_f16 v6, v6, 0
	ds_write_b128 v23, v[6:9]
	ds_read_b128 v[6:9], v26 offset:49152
	s_waitcnt lgkmcnt(0)
	v_pk_max_f16 v10, v9, v9
	s_nop 0
	v_pk_max_f16 v13, v10, 0
	v_pk_max_f16 v10, v8, v8
	buffer_store_dwordx4 v[6:9], v1, s[12:15], 0 offen sc1
	v_pk_max_f16 v12, v10, 0
	v_pk_max_f16 v10, v7, v7
	s_nop 0
	v_pk_max_f16 v11, v10, 0
	v_pk_max_f16 v10, v6, v6
	s_nop 0
	v_pk_max_f16 v10, v10, 0
	ds_write_b128 v26, v[10:13] offset:49152
	v_mov_b32_e32 v10, 0xe000
	v_bitop3_b32 v14, v24, s0, v10 bitop3:0xc8
	s_mul_i32 s0, s3, s18
	v_or_b32_e32 v15, v22, v14
	s_add_i32 s0, s0, s2
	ds_read_b128 v[10:13], v15
	s_mul_i32 s2, s0, 0x60000
	s_mul_hi_i32 s1, s0, 0x60000
	s_add_u32 s2, s6, s2
	s_mulk_i32 s0, 0x300
	s_addc_u32 s3, s7, s1
	s_ashr_i32 s1, s0, 31
	s_lshl_b64 s[0:1], s[0:1], 2
	v_or_b32_e32 v1, v14, v29
	s_add_u32 s4, s8, s0
	s_waitcnt lgkmcnt(0)
	buffer_store_dwordx4 v[10:13], v1, s[12:15], 0 offen sc1
	v_pk_max_f16 v1, v13, v13
	s_addc_u32 s5, s9, s1
	s_mul_i32 s0, s18, 0x1800000
	v_pk_max_f16 v5, v1, 0
	v_pk_max_f16 v1, v12, v12
	s_mul_hi_i32 s1, s18, 0x1800000
	s_add_u32 s0, s10, s0
	v_pk_max_f16 v4, v1, 0
	v_pk_max_f16 v1, v11, v11
	s_addc_u32 s1, s11, s1
	v_pk_max_f16 v3, v1, 0
	v_pk_max_f16 v1, v10, v10
	s_and_b32 s1, s1, 0xffff
	s_mul_i32 s7, s20, 0x6000
	v_pk_max_f16 v2, v1, 0
	v_and_b32_e32 v1, 63, v0
	s_mul_hi_u32 s6, s20, 0x6000
	s_add_u32 s2, s2, s7
	s_addc_u32 s3, s3, s6
	v_lshlrev_b32_e32 v82, 4, v1
	v_lshl_add_u64 v[118:119], s[2:3], 0, v[82:83]
	s_movk_i32 s6, 0x1000
	v_add_co_u32_e32 v50, vcc, s6, v118
	s_movk_i32 s6, 0x2000
	s_nop 0
	v_addc_co_u32_e32 v51, vcc, 0, v119, vcc
	ds_write_b128 v15, v[2:5]
	v_add_co_u32_e32 v52, vcc, s6, v118
	global_load_dwordx4 v[2:5], v82, s[2:3] offset:1024
	global_load_dwordx4 v[6:9], v82, s[2:3] offset:2048
	v_addc_co_u32_e32 v53, vcc, 0, v119, vcc
	global_load_dwordx4 v[10:13], v82, s[2:3] offset:3072
	global_load_dwordx4 v[14:17], v[52:53], off offset:-4096
	global_load_dwordx4 v[18:21], v[50:51], off offset:1024
	global_load_dwordx4 v[22:25], v[50:51], off offset:2048
	global_load_dwordx4 v[26:29], v82, s[2:3]
	global_load_dwordx4 v[30:33], v[50:51], off offset:3072
	global_load_dwordx4 v[34:37], v[52:53], off
	global_load_dwordx4 v[38:41], v[52:53], off offset:1024
	global_load_dwordx4 v[42:45], v[52:53], off offset:2048
	global_load_dwordx4 v[46:49], v[52:53], off offset:3072
	s_movk_i32 s2, 0x3000
	v_add_co_u32_e32 v116, vcc, s2, v118
	s_waitcnt lgkmcnt(0)
	s_nop 0
	v_addc_co_u32_e32 v117, vcc, 0, v119, vcc
	v_add_co_u32_e32 v132, vcc, s21, v118
	s_barrier
	s_nop 0
	v_addc_co_u32_e32 v133, vcc, 0, v119, vcc
	global_load_dwordx4 v[50:53], v[132:133], off offset:-4096
	global_load_dwordx4 v[54:57], v[116:117], off offset:1024
	global_load_dwordx4 v[58:61], v[116:117], off offset:2048
	v_bitop3_b32 v1, v140, v0, 15 bitop3:0x78
	v_lshl_or_b32 v134, v1, 4, v220
	ds_read_b128 v[62:65], v134
	ds_read_b128 v[66:69], v134 offset:8192
	ds_read_b128 v[70:73], v134 offset:16384
	ds_read_b128 v[74:77], v134 offset:24576
	ds_read_b128 v[78:81], v134 offset:32768
	ds_read_b128 v[84:87], v134 offset:40960
	ds_read_b128 v[88:91], v134 offset:49152
	ds_read_b128 v[92:95], v134 offset:57344
	s_mul_i32 s7, s20, 48
	v_lshl_or_b32 v82, v140, 2, s7
	s_mul_i32 s7, s20, 0x60
	s_add_i32 s7, s7, 0x10000
	v_mul_u32_u24_e32 v1, 0x556, v0
	v_lshl_or_b32 v250, v140, 3, s7
	s_or_b32 s7, s16, 64
	v_lshrrev_b32_e32 v143, 16, v1
	s_movk_i32 s6, 0x600
	s_mov_b32 s2, 0x1800000
	s_mov_b32 s3, s15
	v_or_b32_e32 v139, s7, v143
	s_waitcnt vmcnt(8) lgkmcnt(7)
	v_mfma_f32_16x16x32_f16 v[96:99], v[26:29], v[62:65], 0
	s_waitcnt lgkmcnt(6)
	v_mfma_f32_16x16x32_f16 v[100:103], v[26:29], v[66:69], 0
	s_waitcnt lgkmcnt(5)
	v_mfma_f32_16x16x32_f16 v[104:107], v[26:29], v[70:73], 0
	s_waitcnt lgkmcnt(4)
	v_mfma_f32_16x16x32_f16 v[108:111], v[26:29], v[74:77], 0
	s_waitcnt lgkmcnt(3)
	v_mfma_f32_16x16x32_f16 v[112:115], v[26:29], v[78:81], 0
	s_waitcnt lgkmcnt(2)
	v_mfma_f32_16x16x32_f16 v[120:123], v[26:29], v[84:87], 0
	s_waitcnt lgkmcnt(1)
	v_mfma_f32_16x16x32_f16 v[124:127], v[26:29], v[88:91], 0
	s_waitcnt lgkmcnt(0)
	v_mfma_f32_16x16x32_f16 v[26:29], v[26:29], v[92:95], 0
	v_mfma_f32_16x16x32_f16 v[128:131], v[2:5], v[62:65], 0
	v_mfma_f32_16x16x32_f16 v[146:149], v[2:5], v[66:69], 0
	v_mfma_f32_16x16x32_f16 v[150:153], v[2:5], v[70:73], 0
	v_mfma_f32_16x16x32_f16 v[154:157], v[2:5], v[74:77], 0
	v_mfma_f32_16x16x32_f16 v[158:161], v[2:5], v[78:81], 0
	v_mfma_f32_16x16x32_f16 v[162:165], v[2:5], v[84:87], 0
	v_mfma_f32_16x16x32_f16 v[166:169], v[2:5], v[88:91], 0
	v_mfma_f32_16x16x32_f16 v[2:5], v[2:5], v[92:95], 0
	v_mfma_f32_16x16x32_f16 v[62:65], v[6:9], v[62:65], 0
	v_mfma_f32_16x16x32_f16 v[66:69], v[6:9], v[66:69], 0
	v_mfma_f32_16x16x32_f16 v[70:73], v[6:9], v[70:73], 0
	v_mfma_f32_16x16x32_f16 v[74:77], v[6:9], v[74:77], 0
	v_mfma_f32_16x16x32_f16 v[78:81], v[6:9], v[78:81], 0
	v_mfma_f32_16x16x32_f16 v[84:87], v[6:9], v[84:87], 0
	v_mfma_f32_16x16x32_f16 v[88:91], v[6:9], v[88:91], 0
	v_mfma_f32_16x16x32_f16 v[6:9], v[6:9], v[92:95], 0
	global_load_dwordx4 v[92:95], v[116:117], off offset:3072
	global_load_dwordx4 v[170:173], v[132:133], off
	global_load_dwordx4 v[174:177], v[132:133], off offset:1024
	v_bitop3_b32 v1, v140, v145, 4 bitop3:0x36
	v_lshl_or_b32 v1, v1, 4, v220
	ds_read_b128 v[178:181], v1
	ds_read_b128 v[182:185], v1 offset:8192
	ds_read_b128 v[186:189], v1 offset:16384
	ds_read_b128 v[190:193], v1 offset:24576
	ds_read_b128 v[194:197], v1 offset:32768
	ds_read_b128 v[198:201], v1 offset:40960
	ds_read_b128 v[202:205], v1 offset:49152
	ds_read_b128 v[206:209], v1 offset:57344
	s_waitcnt lgkmcnt(7)
	v_mfma_f32_16x16x32_f16 v[96:99], v[10:13], v[178:181], v[96:99]
	s_waitcnt lgkmcnt(6)
	v_mfma_f32_16x16x32_f16 v[100:103], v[10:13], v[182:185], v[100:103]
	s_waitcnt lgkmcnt(5)
	v_mfma_f32_16x16x32_f16 v[104:107], v[10:13], v[186:189], v[104:107]
	s_waitcnt lgkmcnt(4)
	v_mfma_f32_16x16x32_f16 v[108:111], v[10:13], v[190:193], v[108:111]
	s_waitcnt lgkmcnt(3)
	v_mfma_f32_16x16x32_f16 v[112:115], v[10:13], v[194:197], v[112:115]
	s_waitcnt lgkmcnt(2)
	v_mfma_f32_16x16x32_f16 v[120:123], v[10:13], v[198:201], v[120:123]
	s_waitcnt lgkmcnt(1)
	v_mfma_f32_16x16x32_f16 v[124:127], v[10:13], v[202:205], v[124:127]
	s_waitcnt lgkmcnt(0)
	v_mfma_f32_16x16x32_f16 v[10:13], v[10:13], v[206:209], v[26:29]
	v_mfma_f32_16x16x32_f16 v[26:29], v[14:17], v[178:181], v[128:131]
	v_mfma_f32_16x16x32_f16 v[128:131], v[14:17], v[182:185], v[146:149]
	v_mfma_f32_16x16x32_f16 v[146:149], v[14:17], v[186:189], v[150:153]
	v_mfma_f32_16x16x32_f16 v[150:153], v[14:17], v[190:193], v[154:157]
	v_mfma_f32_16x16x32_f16 v[154:157], v[14:17], v[194:197], v[158:161]
	v_mfma_f32_16x16x32_f16 v[158:161], v[14:17], v[198:201], v[162:165]
	v_mfma_f32_16x16x32_f16 v[162:165], v[14:17], v[202:205], v[166:169]
	v_mfma_f32_16x16x32_f16 v[2:5], v[14:17], v[206:209], v[2:5]
	v_mfma_f32_16x16x32_f16 v[14:17], v[18:21], v[178:181], v[62:65]
	v_mfma_f32_16x16x32_f16 v[62:65], v[18:21], v[182:185], v[66:69]
	v_mfma_f32_16x16x32_f16 v[66:69], v[18:21], v[186:189], v[70:73]
	v_mfma_f32_16x16x32_f16 v[70:73], v[18:21], v[190:193], v[74:77]
	v_mfma_f32_16x16x32_f16 v[74:77], v[18:21], v[194:197], v[78:81]
	v_mfma_f32_16x16x32_f16 v[78:81], v[18:21], v[198:201], v[84:87]
	v_mfma_f32_16x16x32_f16 v[84:87], v[18:21], v[202:205], v[88:91]
	v_mfma_f32_16x16x32_f16 v[6:9], v[18:21], v[206:209], v[6:9]
	s_movk_i32 s8, 0x5000
	v_add_co_u32_e32 v116, vcc, s8, v118
	global_load_dwordx4 v[88:91], v[132:133], off offset:2048
	global_load_dwordx4 v[166:169], v[132:133], off offset:3072
	v_addc_co_u32_e32 v117, vcc, 0, v119, vcc
	global_load_dwordx4 v[178:181], v[116:117], off
	v_bitop3_b32 v18, v140, v145, 8 bitop3:0x36
	v_lshl_or_b32 v133, v18, 4, v220
	ds_read_b128 v[18:21], v133
	ds_read_b128 v[182:185], v133 offset:8192
	ds_read_b128 v[186:189], v133 offset:16384
	ds_read_b128 v[190:193], v133 offset:24576
	ds_read_b128 v[194:197], v133 offset:32768
	ds_read_b128 v[198:201], v133 offset:40960
	ds_read_b128 v[202:205], v133 offset:49152
	ds_read_b128 v[206:209], v133 offset:57344
	s_waitcnt lgkmcnt(7)
	v_mfma_f32_16x16x32_f16 v[96:99], v[22:25], v[18:21], v[96:99]
	s_waitcnt lgkmcnt(6)
	v_mfma_f32_16x16x32_f16 v[100:103], v[22:25], v[182:185], v[100:103]
	s_waitcnt lgkmcnt(5)
	v_mfma_f32_16x16x32_f16 v[104:107], v[22:25], v[186:189], v[104:107]
	s_waitcnt lgkmcnt(4)
	v_mfma_f32_16x16x32_f16 v[108:111], v[22:25], v[190:193], v[108:111]
	s_waitcnt lgkmcnt(3)
	v_mfma_f32_16x16x32_f16 v[112:115], v[22:25], v[194:197], v[112:115]
	s_waitcnt lgkmcnt(2)
	v_mfma_f32_16x16x32_f16 v[120:123], v[22:25], v[198:201], v[120:123]
	s_waitcnt lgkmcnt(1)
	v_mfma_f32_16x16x32_f16 v[124:127], v[22:25], v[202:205], v[124:127]
	s_waitcnt lgkmcnt(0)
	v_mfma_f32_16x16x32_f16 v[10:13], v[22:25], v[206:209], v[10:13]
	s_waitcnt vmcnt(13)
	v_mfma_f32_16x16x32_f16 v[22:25], v[30:33], v[18:21], v[26:29]
	v_mfma_f32_16x16x32_f16 v[26:29], v[30:33], v[182:185], v[128:131]
	v_mfma_f32_16x16x32_f16 v[128:131], v[30:33], v[186:189], v[146:149]
	v_mfma_f32_16x16x32_f16 v[146:149], v[30:33], v[190:193], v[150:153]
	v_mfma_f32_16x16x32_f16 v[150:153], v[30:33], v[194:197], v[154:157]
	v_mfma_f32_16x16x32_f16 v[154:157], v[30:33], v[198:201], v[158:161]
	v_mfma_f32_16x16x32_f16 v[158:161], v[30:33], v[202:205], v[162:165]
	v_mfma_f32_16x16x32_f16 v[2:5], v[30:33], v[206:209], v[2:5]
	s_waitcnt vmcnt(12)
	v_mfma_f32_16x16x32_f16 v[14:17], v[34:37], v[18:21], v[14:17]
	v_mfma_f32_16x16x32_f16 v[18:21], v[34:37], v[182:185], v[62:65]
	v_mfma_f32_16x16x32_f16 v[30:33], v[34:37], v[186:189], v[66:69]
	v_mfma_f32_16x16x32_f16 v[62:65], v[34:37], v[190:193], v[70:73]
	v_mfma_f32_16x16x32_f16 v[66:69], v[34:37], v[194:197], v[74:77]
	v_mfma_f32_16x16x32_f16 v[70:73], v[34:37], v[198:201], v[78:81]
	v_mfma_f32_16x16x32_f16 v[74:77], v[34:37], v[202:205], v[84:87]
	v_mfma_f32_16x16x32_f16 v[6:9], v[34:37], v[206:209], v[6:9]
	s_nop 0
	global_load_dwordx4 v[78:81], v[116:117], off offset:1024
	global_load_dwordx4 v[162:165], v[116:117], off offset:2048
	global_load_dwordx4 v[182:185], v[116:117], off offset:3072
	v_bitop3_b32 v34, v140, v145, 12 bitop3:0x36
	v_lshl_or_b32 v135, v34, 4, v220
	ds_read_b128 v[34:37], v135
	ds_read_b128 v[84:87], v135 offset:8192
	ds_read_b128 v[186:189], v135 offset:16384
	ds_read_b128 v[190:193], v135 offset:24576
	ds_read_b128 v[194:197], v135 offset:32768
	ds_read_b128 v[198:201], v135 offset:40960
	ds_read_b128 v[202:205], v135 offset:49152
	ds_read_b128 v[206:209], v135 offset:57344
	s_waitcnt vmcnt(14) lgkmcnt(7)
	v_mfma_f32_16x16x32_f16 v[96:99], v[38:41], v[34:37], v[96:99]
	s_waitcnt lgkmcnt(6)
	v_mfma_f32_16x16x32_f16 v[100:103], v[38:41], v[84:87], v[100:103]
	s_waitcnt lgkmcnt(5)
	v_mfma_f32_16x16x32_f16 v[104:107], v[38:41], v[186:189], v[104:107]
	s_waitcnt lgkmcnt(4)
	v_mfma_f32_16x16x32_f16 v[108:111], v[38:41], v[190:193], v[108:111]
	s_waitcnt lgkmcnt(3)
	v_mfma_f32_16x16x32_f16 v[112:115], v[38:41], v[194:197], v[112:115]
	s_waitcnt lgkmcnt(2)
	v_mfma_f32_16x16x32_f16 v[120:123], v[38:41], v[198:201], v[120:123]
	s_waitcnt lgkmcnt(1)
	v_mfma_f32_16x16x32_f16 v[124:127], v[38:41], v[202:205], v[124:127]
	s_waitcnt lgkmcnt(0)
	v_mfma_f32_16x16x32_f16 v[210:213], v[38:41], v[206:209], v[10:13]
	s_waitcnt vmcnt(13)
	v_mfma_f32_16x16x32_f16 v[22:25], v[42:45], v[34:37], v[22:25]
	v_mfma_f32_16x16x32_f16 v[214:217], v[42:45], v[84:87], v[26:29]
	v_mfma_f32_16x16x32_f16 v[128:131], v[42:45], v[186:189], v[128:131]
	v_mfma_f32_16x16x32_f16 v[146:149], v[42:45], v[190:193], v[146:149]
	v_mfma_f32_16x16x32_f16 v[150:153], v[42:45], v[194:197], v[150:153]
	v_mfma_f32_16x16x32_f16 v[154:157], v[42:45], v[198:201], v[154:157]
	v_mfma_f32_16x16x32_f16 v[158:161], v[42:45], v[202:205], v[158:161]
	v_mfma_f32_16x16x32_f16 v[2:5], v[42:45], v[206:209], v[2:5]
	s_waitcnt vmcnt(12)
	v_mfma_f32_16x16x32_f16 v[14:17], v[46:49], v[34:37], v[14:17]
	v_mfma_f32_16x16x32_f16 v[18:21], v[46:49], v[84:87], v[18:21]
	v_mfma_f32_16x16x32_f16 v[30:33], v[46:49], v[186:189], v[30:33]
	v_mfma_f32_16x16x32_f16 v[34:37], v[46:49], v[190:193], v[62:65]
	v_mfma_f32_16x16x32_f16 v[42:45], v[46:49], v[194:197], v[66:69]
	v_mfma_f32_16x16x32_f16 v[62:65], v[46:49], v[198:201], v[70:73]
	v_mfma_f32_16x16x32_f16 v[66:69], v[46:49], v[202:205], v[74:77]
	v_mfma_f32_16x16x32_f16 v[6:9], v[46:49], v[206:209], v[6:9]
	s_mov_b32 s8, 0x30000
	v_add_co_u32_e32 v116, vcc, s8, v118
	s_mov_b32 s8, 0x31000
	s_nop 0
	v_addc_co_u32_e32 v117, vcc, 0, v119, vcc
	v_add_co_u32_e32 v218, vcc, s8, v118
	v_bitop3_b32 v46, v140, v145, 16 bitop3:0x36
	s_nop 0
	v_addc_co_u32_e32 v219, vcc, 0, v119, vcc
	global_load_dwordx4 v[38:41], v[218:219], off offset:-4096
	global_load_dwordx4 v[26:29], v[116:117], off offset:1024
	global_load_dwordx4 v[10:13], v[116:117], off offset:2048
	v_lshl_or_b32 v136, v46, 4, v220
	ds_read_b128 v[46:49], v136
	ds_read_b128 v[70:73], v136 offset:8192
	ds_read_b128 v[74:77], v136 offset:16384
	ds_read_b128 v[84:87], v136 offset:24576
	ds_read_b128 v[186:189], v136 offset:32768
	ds_read_b128 v[190:193], v136 offset:40960
	ds_read_b128 v[194:197], v136 offset:49152
	ds_read_b128 v[198:201], v136 offset:57344
	s_waitcnt vmcnt(14) lgkmcnt(7)
	v_mfma_f32_16x16x32_f16 v[96:99], v[50:53], v[46:49], v[96:99]
	s_waitcnt lgkmcnt(6)
	v_mfma_f32_16x16x32_f16 v[100:103], v[50:53], v[70:73], v[100:103]
	s_waitcnt lgkmcnt(5)
	v_mfma_f32_16x16x32_f16 v[104:107], v[50:53], v[74:77], v[104:107]
	s_waitcnt lgkmcnt(4)
	v_mfma_f32_16x16x32_f16 v[108:111], v[50:53], v[84:87], v[108:111]
	s_waitcnt lgkmcnt(3)
	v_mfma_f32_16x16x32_f16 v[112:115], v[50:53], v[186:189], v[112:115]
	s_waitcnt lgkmcnt(2)
	v_mfma_f32_16x16x32_f16 v[120:123], v[50:53], v[190:193], v[120:123]
	s_waitcnt lgkmcnt(1)
	v_mfma_f32_16x16x32_f16 v[124:127], v[50:53], v[194:197], v[124:127]
	s_waitcnt lgkmcnt(0)
	v_mfma_f32_16x16x32_f16 v[50:53], v[50:53], v[198:201], v[210:213]
	s_waitcnt vmcnt(13)
	v_mfma_f32_16x16x32_f16 v[202:205], v[54:57], v[46:49], v[22:25]
	v_mfma_f32_16x16x32_f16 v[206:209], v[54:57], v[70:73], v[214:217]
	v_mfma_f32_16x16x32_f16 v[128:131], v[54:57], v[74:77], v[128:131]
	v_mfma_f32_16x16x32_f16 v[146:149], v[54:57], v[84:87], v[146:149]
	v_mfma_f32_16x16x32_f16 v[150:153], v[54:57], v[186:189], v[150:153]
	v_mfma_f32_16x16x32_f16 v[154:157], v[54:57], v[190:193], v[154:157]
	v_mfma_f32_16x16x32_f16 v[158:161], v[54:57], v[194:197], v[158:161]
	v_mfma_f32_16x16x32_f16 v[54:57], v[54:57], v[198:201], v[2:5]
	s_waitcnt vmcnt(12)
	v_mfma_f32_16x16x32_f16 v[14:17], v[58:61], v[46:49], v[14:17]
	v_mfma_f32_16x16x32_f16 v[18:21], v[58:61], v[70:73], v[18:21]
	v_mfma_f32_16x16x32_f16 v[30:33], v[58:61], v[74:77], v[30:33]
	v_mfma_f32_16x16x32_f16 v[34:37], v[58:61], v[84:87], v[34:37]
	v_mfma_f32_16x16x32_f16 v[42:45], v[58:61], v[186:189], v[42:45]
	v_mfma_f32_16x16x32_f16 v[46:49], v[58:61], v[190:193], v[62:65]
	v_mfma_f32_16x16x32_f16 v[62:65], v[58:61], v[194:197], v[66:69]
	v_mfma_f32_16x16x32_f16 v[58:61], v[58:61], v[198:201], v[6:9]
	global_load_dwordx4 v[22:25], v[116:117], off offset:3072
	s_nop 1
	global_load_dwordx4 v[6:9], v[218:219], off
	global_load_dwordx4 v[2:5], v[218:219], off offset:1024
	v_bitop3_b32 v66, v140, v145, 20 bitop3:0x36
	v_lshl_or_b32 v137, v66, 4, v220
	ds_read_b128 v[66:69], v137
	ds_read_b128 v[70:73], v137 offset:8192
	ds_read_b128 v[74:77], v137 offset:16384
	ds_read_b128 v[84:87], v137 offset:24576
	ds_read_b128 v[186:189], v137 offset:32768
	ds_read_b128 v[190:193], v137 offset:40960
	ds_read_b128 v[194:197], v137 offset:49152
	ds_read_b128 v[198:201], v137 offset:57344
	s_waitcnt vmcnt(14) lgkmcnt(7)
	v_mfma_f32_16x16x32_f16 v[96:99], v[92:95], v[66:69], v[96:99]
	s_waitcnt lgkmcnt(6)
	v_mfma_f32_16x16x32_f16 v[100:103], v[92:95], v[70:73], v[100:103]
	s_waitcnt lgkmcnt(5)
	v_mfma_f32_16x16x32_f16 v[104:107], v[92:95], v[74:77], v[104:107]
	s_waitcnt lgkmcnt(4)
	v_mfma_f32_16x16x32_f16 v[108:111], v[92:95], v[84:87], v[108:111]
	s_waitcnt lgkmcnt(3)
	v_mfma_f32_16x16x32_f16 v[112:115], v[92:95], v[186:189], v[112:115]
	s_waitcnt lgkmcnt(2)
	v_mfma_f32_16x16x32_f16 v[210:213], v[92:95], v[190:193], v[120:123]
	s_waitcnt lgkmcnt(1)
	v_mfma_f32_16x16x32_f16 v[124:127], v[92:95], v[194:197], v[124:127]
	s_waitcnt lgkmcnt(0)
	v_mfma_f32_16x16x32_f16 v[50:53], v[92:95], v[198:201], v[50:53]
	s_waitcnt vmcnt(13)
	v_mfma_f32_16x16x32_f16 v[92:95], v[170:173], v[66:69], v[202:205]
	v_mfma_f32_16x16x32_f16 v[202:205], v[170:173], v[70:73], v[206:209]
	v_mfma_f32_16x16x32_f16 v[128:131], v[170:173], v[74:77], v[128:131]
	v_mfma_f32_16x16x32_f16 v[146:149], v[170:173], v[84:87], v[146:149]
	v_mfma_f32_16x16x32_f16 v[150:153], v[170:173], v[186:189], v[150:153]
	v_mfma_f32_16x16x32_f16 v[154:157], v[170:173], v[190:193], v[154:157]
	v_mfma_f32_16x16x32_f16 v[158:161], v[170:173], v[194:197], v[158:161]
	v_mfma_f32_16x16x32_f16 v[54:57], v[170:173], v[198:201], v[54:57]
	s_waitcnt vmcnt(12)
	v_mfma_f32_16x16x32_f16 v[66:69], v[174:177], v[66:69], v[14:17]
	v_mfma_f32_16x16x32_f16 v[70:73], v[174:177], v[70:73], v[18:21]
	v_mfma_f32_16x16x32_f16 v[74:77], v[174:177], v[74:77], v[30:33]
	v_mfma_f32_16x16x32_f16 v[34:37], v[174:177], v[84:87], v[34:37]
	v_mfma_f32_16x16x32_f16 v[42:45], v[174:177], v[186:189], v[42:45]
	v_mfma_f32_16x16x32_f16 v[46:49], v[174:177], v[190:193], v[46:49]
	v_mfma_f32_16x16x32_f16 v[62:65], v[174:177], v[194:197], v[62:65]
	v_mfma_f32_16x16x32_f16 v[58:61], v[174:177], v[198:201], v[58:61]
	s_mov_b32 s8, 0x33000
	v_add_co_u32_e32 v122, vcc, s8, v118
	global_load_dwordx4 v[30:33], v[218:219], off offset:2048
	global_load_dwordx4 v[14:17], v[218:219], off offset:3072
	v_addc_co_u32_e32 v123, vcc, 0, v119, vcc
	global_load_dwordx4 v[18:21], v[122:123], off offset:-4096
	v_bitop3_b32 v84, v140, v145, 24 bitop3:0x36
	v_lshl_or_b32 v138, v84, 4, v220
	ds_read_b128 v[84:87], v138
	ds_read_b128 v[170:173], v138 offset:8192
	ds_read_b128 v[174:177], v138 offset:16384
	ds_read_b128 v[186:189], v138 offset:24576
	ds_read_b128 v[190:193], v138 offset:32768
	ds_read_b128 v[194:197], v138 offset:40960
	ds_read_b128 v[198:201], v138 offset:49152
	ds_read_b128 v[206:209], v138 offset:57344
	s_mov_b32 s8, 0x32000
	v_add_co_u32_e32 v116, vcc, s8, v118
	s_nop 1
	v_addc_co_u32_e32 v117, vcc, 0, v119, vcc
	s_waitcnt vmcnt(14) lgkmcnt(7)
	v_mfma_f32_16x16x32_f16 v[96:99], v[88:91], v[84:87], v[96:99]
	s_waitcnt lgkmcnt(6)
	v_mfma_f32_16x16x32_f16 v[100:103], v[88:91], v[170:173], v[100:103]
	s_waitcnt lgkmcnt(5)
	v_mfma_f32_16x16x32_f16 v[104:107], v[88:91], v[174:177], v[104:107]
	s_waitcnt lgkmcnt(4)
	v_mfma_f32_16x16x32_f16 v[108:111], v[88:91], v[186:189], v[108:111]
	s_waitcnt lgkmcnt(3)
	v_mfma_f32_16x16x32_f16 v[112:115], v[88:91], v[190:193], v[112:115]
	s_waitcnt lgkmcnt(2)
	v_mfma_f32_16x16x32_f16 v[210:213], v[88:91], v[194:197], v[210:213]
	s_waitcnt lgkmcnt(1)
	v_mfma_f32_16x16x32_f16 v[124:127], v[88:91], v[198:201], v[124:127]
	s_waitcnt lgkmcnt(0)
	v_mfma_f32_16x16x32_f16 v[50:53], v[88:91], v[206:209], v[50:53]
	s_waitcnt vmcnt(13)
	v_mfma_f32_16x16x32_f16 v[90:93], v[166:169], v[84:87], v[92:95]
	v_mfma_f32_16x16x32_f16 v[202:205], v[166:169], v[170:173], v[202:205]
	v_mfma_f32_16x16x32_f16 v[128:131], v[166:169], v[174:177], v[128:131]
	v_mfma_f32_16x16x32_f16 v[146:149], v[166:169], v[186:189], v[146:149]
	v_mfma_f32_16x16x32_f16 v[150:153], v[166:169], v[190:193], v[150:153]
	v_mfma_f32_16x16x32_f16 v[154:157], v[166:169], v[194:197], v[154:157]
	v_mfma_f32_16x16x32_f16 v[158:161], v[166:169], v[198:201], v[158:161]
	v_mfma_f32_16x16x32_f16 v[54:57], v[166:169], v[206:209], v[54:57]
	s_waitcnt vmcnt(12)
	v_mfma_f32_16x16x32_f16 v[166:169], v[178:181], v[84:87], v[66:69]
	v_mfma_f32_16x16x32_f16 v[170:173], v[178:181], v[170:173], v[70:73]
	v_mfma_f32_16x16x32_f16 v[174:177], v[178:181], v[174:177], v[74:77]
	v_mfma_f32_16x16x32_f16 v[186:189], v[178:181], v[186:189], v[34:37]
	v_mfma_f32_16x16x32_f16 v[190:193], v[178:181], v[190:193], v[42:45]
	v_mfma_f32_16x16x32_f16 v[194:197], v[178:181], v[194:197], v[46:49]
	v_mfma_f32_16x16x32_f16 v[198:201], v[178:181], v[198:201], v[62:65]
	v_mfma_f32_16x16x32_f16 v[178:181], v[178:181], v[206:209], v[58:61]
	s_nop 0
	global_load_dwordx4 v[46:49], v[116:117], off offset:1024
	global_load_dwordx4 v[42:45], v[116:117], off offset:2048
	global_load_dwordx4 v[34:37], v[116:117], off offset:3072
	v_bitop3_b32 v58, v140, v145, 28 bitop3:0x36
	v_lshl_or_b32 v140, v58, 4, v220
	ds_read_b128 v[58:61], v140
	ds_read_b128 v[62:65], v140 offset:8192
	ds_read_b128 v[206:209], v140 offset:16384
	ds_read_b128 v[214:217], v140 offset:24576
	ds_read_b128 v[218:221], v140 offset:32768
	ds_read_b128 v[222:225], v140 offset:40960
	ds_read_b128 v[226:229], v140 offset:49152
	ds_read_b128 v[230:233], v140 offset:57344
	s_waitcnt vmcnt(14) lgkmcnt(7)
	v_mfma_f32_16x16x32_f16 v[234:237], v[78:81], v[58:61], v[96:99]
	s_waitcnt lgkmcnt(6)
	v_mfma_f32_16x16x32_f16 v[238:241], v[78:81], v[62:65], v[100:103]
	s_waitcnt lgkmcnt(5)
	v_mfma_f32_16x16x32_f16 v[242:245], v[78:81], v[206:209], v[104:107]
	s_waitcnt lgkmcnt(4)
	v_mfma_f32_16x16x32_f16 v[246:249], v[78:81], v[214:217], v[108:111]
	s_waitcnt lgkmcnt(3)
	v_mfma_f32_16x16x32_f16 v[106:109], v[78:81], v[218:221], v[112:115]
	s_waitcnt lgkmcnt(2)
	v_mfma_f32_16x16x32_f16 v[102:105], v[78:81], v[222:225], v[210:213]
	s_waitcnt lgkmcnt(1)
	v_mfma_f32_16x16x32_f16 v[94:97], v[78:81], v[226:229], v[124:127]
	s_waitcnt lgkmcnt(0)
	v_mfma_f32_16x16x32_f16 v[86:89], v[78:81], v[230:233], v[50:53]
	s_waitcnt vmcnt(13)
	v_mfma_f32_16x16x32_f16 v[124:127], v[162:165], v[58:61], v[90:93]
	v_mfma_f32_16x16x32_f16 v[202:205], v[162:165], v[62:65], v[202:205]
	v_mfma_f32_16x16x32_f16 v[210:213], v[162:165], v[206:209], v[128:131]
	v_mfma_f32_16x16x32_f16 v[146:149], v[162:165], v[214:217], v[146:149]
	v_mfma_f32_16x16x32_f16 v[78:81], v[162:165], v[218:221], v[150:153]
	v_mfma_f32_16x16x32_f16 v[74:77], v[162:165], v[222:225], v[154:157]
	v_mfma_f32_16x16x32_f16 v[70:73], v[162:165], v[226:229], v[158:161]
	v_mfma_f32_16x16x32_f16 v[66:69], v[162:165], v[230:233], v[54:57]
	s_waitcnt vmcnt(12)
	v_mfma_f32_16x16x32_f16 v[150:153], v[182:185], v[58:61], v[166:169]
	v_mfma_f32_16x16x32_f16 v[154:157], v[182:185], v[62:65], v[170:173]
	v_mfma_f32_16x16x32_f16 v[114:117], v[182:185], v[206:209], v[174:177]
	v_mfma_f32_16x16x32_f16 v[110:113], v[182:185], v[214:217], v[186:189]
	v_mfma_f32_16x16x32_f16 v[62:65], v[182:185], v[218:221], v[190:193]
	v_mfma_f32_16x16x32_f16 v[58:61], v[182:185], v[222:225], v[194:197]
	v_mfma_f32_16x16x32_f16 v[54:57], v[182:185], v[226:229], v[198:201]
	v_mfma_f32_16x16x32_f16 v[50:53], v[182:185], v[230:233], v[178:181]
	v_lshl_add_u64 v[120:121], v[82:83], 2, s[4:5]
	global_load_dwordx4 v[98:101], v[120:121], off
	global_load_dwordx4 v[90:93], v[120:121], off offset:64
	global_load_dwordx4 v[82:85], v[120:121], off offset:128
	s_movk_i32 s5, 0x310
	v_mad_u32_u24 v130, v145, s5, v250
	v_mov_b32_e32 v158, v239
	v_mov_b32_e32 v159, v240
	v_mov_b32_e32 v160, v243
	v_mov_b32_e32 v161, v244
	v_mov_b32_e32 v162, v247
	v_mov_b32_e32 v163, v248
	v_mov_b32_e32 v164, v203
	v_mov_b32_e32 v165, v204
	v_mov_b32_e32 v169, v148
	v_mov_b32_e32 v166, v211
	v_mov_b32_e32 v167, v212
	v_mov_b32_e32 v168, v147
	s_barrier
	v_add_u32_e32 v132, 0x3000, v130
	v_add_u32_e32 v131, 0x6000, v130
	s_mov_b32 s4, 0xfffffd0
	v_mul_lo_u32 v176, v143, s4
	s_waitcnt vmcnt(2)
	v_pk_add_f32 v[170:171], v[234:235], v[98:99]
	v_pk_add_f32 v[172:173], v[236:237], v[100:101]
	v_add_f32_e32 v145, v238, v98
	v_pk_mov_b32 v[128:129], v[98:99], v[100:101] op_sel:[1,0]
	v_add_f32_e32 v99, v241, v101
	s_waitcnt vmcnt(1)
	v_pk_add_f32 v[124:125], v[124:125], v[90:91]
	v_pk_add_f32 v[174:175], v[126:127], v[92:93]
	v_add_f32_e32 v180, v202, v90
	v_pk_mov_b32 v[126:127], v[90:91], v[92:93] op_sel:[1,0]
	v_add_f32_e32 v91, v205, v93
	v_add_f32_e32 v100, v242, v98
	v_add_f32_e32 v177, v245, v101
	v_add_f32_e32 v92, v210, v90
	v_add_f32_e32 v181, v213, v93
	v_add_f32_e32 v183, v149, v93
	v_cvt_pk_f16_f32 v149, v172, v173
	v_cvt_f16_f32_e32 v145, v145
	v_cvt_f16_f32_e32 v99, v99
	v_cvt_f16_f32_e32 v173, v180
	v_cvt_f16_f32_e32 v91, v91
	v_cvt_pk_f16_f32 v148, v170, v171
	v_cvt_f16_f32_e32 v100, v100
	v_cvt_f16_f32_e32 v170, v177
	v_cvt_pk_f16_f32 v124, v124, v125
	v_cvt_pk_f16_f32 v125, v174, v175
	v_cvt_f16_f32_e32 v92, v92
	v_cvt_f16_f32_e32 v174, v181
	v_add_f32_e32 v182, v146, v90
	s_waitcnt vmcnt(0)
	v_pk_add_f32 v[146:147], v[150:151], v[82:83]
	v_pk_add_f32 v[150:151], v[158:159], v[128:129]
	v_pk_add_f32 v[158:159], v[160:161], v[128:129]
	v_pk_add_f32 v[160:161], v[162:163], v[128:129]
	v_pk_add_f32 v[162:163], v[164:165], v[126:127]
	v_pk_add_f32 v[164:165], v[166:167], v[126:127]
	v_cvt_pk_f16_f32 v146, v146, v147
	v_cvt_pk_f16_f32 v147, v150, v151
	v_cvt_pk_f16_f32 v150, v158, v159
	v_cvt_pk_f16_f32 v159, v162, v163
	v_cvt_pk_f16_f32 v151, v160, v161
	v_cvt_pk_f16_f32 v161, v164, v165
	ds_write2_b64 v130, v[148:149], v[124:125] offset1:4
	v_pack_b32_f16 v124, v145, v147
	v_alignbit_b32 v125, v99, v147, 16
	v_pack_b32_f16 v158, v173, v159
	v_alignbit_b32 v159, v91, v159, 16
	v_pack_b32_f16 v148, v100, v150
	v_alignbit_b32 v149, v170, v150, 16
	v_pack_b32_f16 v160, v92, v161
	v_alignbit_b32 v161, v174, v161, 16
	ds_write2_b64 v132, v[124:125], v[158:159] offset0:32 offset1:36
	ds_write2_b64 v131, v[148:149], v[160:161] offset0:64 offset1:68
	v_pk_add_f32 v[124:125], v[152:153], v[84:85]
	v_add_f32_e32 v92, v154, v82
	v_cvt_pk_f16_f32 v147, v124, v125
	v_pk_mov_b32 v[124:125], v[82:83], v[84:85] op_sel:[1,0]
	v_add_f32_e32 v83, v157, v85
	v_cvt_f16_f32_e32 v92, v92
	v_cvt_f16_f32_e32 v83, v83
	ds_write_b64 v130, v[146:147] offset:64
	v_mov_b32_e32 v146, v155
	v_mov_b32_e32 v147, v156
	v_pk_add_f32 v[146:147], v[146:147], v[124:125]
	v_add_f32_e32 v178, v246, v98
	v_cvt_pk_f16_f32 v84, v146, v147
	v_pack_b32_f16 v146, v92, v84
	v_alignbit_b32 v147, v83, v84, 16
	v_add_f32_e32 v83, v114, v82
	v_add_f32_e32 v84, v117, v85
	v_cvt_f16_f32_e32 v83, v83
	v_cvt_f16_f32_e32 v84, v84
	v_mov_b32_e32 v114, v115
	v_mov_b32_e32 v115, v116
	v_pk_add_f32 v[114:115], v[114:115], v[124:125]
	v_add_f32_e32 v179, v249, v101
	v_cvt_pk_f16_f32 v92, v114, v115
	v_pack_b32_f16 v114, v83, v92
	v_alignbit_b32 v115, v84, v92, 16
	v_add_f32_e32 v83, v110, v82
	v_add_f32_e32 v84, v113, v85
	v_cvt_f16_f32_e32 v83, v83
	v_cvt_f16_f32_e32 v84, v84
	v_mov_b32_e32 v110, v111
	v_mov_b32_e32 v111, v112
	v_cvt_f16_f32_e32 v171, v178
	v_cvt_f16_f32_e32 v172, v179
	v_cvt_f16_f32_e32 v175, v182
	v_pk_add_f32 v[166:167], v[168:169], v[126:127]
	v_cvt_f16_f32_e32 v168, v183
	v_pk_add_f32 v[110:111], v[110:111], v[124:125]
	v_cvt_pk_f16_f32 v163, v166, v167
	v_cvt_pk_f16_f32 v92, v110, v111
	v_pack_b32_f16 v110, v83, v92
	v_alignbit_b32 v111, v84, v92, 16
	v_or_b32_e32 v83, s16, v143
	ds_write_b64 v130, v[110:111] offset:37696
	v_add_lshl_u32 v111, v176, v0, 4
	v_mul_lo_u32 v112, v83, s6
	v_mul_u32_u24_e32 v83, 0x310, v143
	v_mul_u32_u24_e32 v84, 0x556, v141
	v_pack_b32_f16 v150, v171, v151
	v_alignbit_b32 v151, v172, v151, 16
	v_pack_b32_f16 v162, v175, v163
	v_alignbit_b32 v163, v168, v163, 16
	v_add_u32_e32 v91, 0x9000, v130
	v_add3_u32 v83, v111, v83, s14
	v_lshrrev_b32_e32 v154, 16, v84
	ds_write2_b64 v91, v[150:151], v[162:163] offset0:96 offset1:100
	ds_write_b64 v130, v[146:147] offset:12608
	ds_write_b64 v130, v[114:115] offset:25152
	s_waitcnt lgkmcnt(0)
	s_barrier
	ds_read_b128 v[114:117], v83
	v_mul_lo_u32 v84, v154, s4
	v_add_lshl_u32 v113, v84, v141, 4
	v_mul_u32_u24_e32 v84, 0x310, v154
	v_add3_u32 v84, v113, v84, s14
	ds_read_b128 v[146:149], v84
	v_add_u32_e32 v92, v111, v112
	s_waitcnt lgkmcnt(1)
	buffer_store_dwordx4 v[114:117], v92, s[0:3], 0 offen sc1
	v_or_b32_e32 v92, s16, v154
	s_nop 0
	v_mul_lo_u32 v114, v92, s6
	v_add_u32_e32 v92, v113, v114
	s_waitcnt lgkmcnt(0)
	buffer_store_dwordx4 v[146:149], v92, s[0:3], 0 offen sc1
	v_or_b32_e32 v92, 0x400, v0
	v_mul_u32_u24_e32 v99, 0x556, v92
	v_lshrrev_b32_e32 v155, 16, v99
	v_mul_lo_u32 v99, v155, s4
	v_add_lshl_u32 v115, v99, v92, 4
	v_mul_u32_u24_e32 v92, 0x310, v155
	v_mul_u32_u24_e32 v99, 0x556, v142
	v_add3_u32 v92, v115, v92, s14
	v_lshrrev_b32_e32 v156, 16, v99
	ds_read_b128 v[146:149], v92
	v_mul_lo_u32 v99, v156, s4
	v_add_lshl_u32 v117, v99, v142, 4
	v_mul_u32_u24_e32 v99, 0x310, v156
	v_or_b32_e32 v100, s16, v155
	v_add3_u32 v99, v117, v99, s14
	v_mul_lo_u32 v116, v100, s6
	ds_read_b128 v[150:153], v99
	v_add_u32_e32 v100, v115, v116
	s_waitcnt lgkmcnt(1)
	buffer_store_dwordx4 v[146:149], v100, s[0:3], 0 offen sc1
	v_or_b32_e32 v100, s16, v156
	v_mul_lo_u32 v142, v100, s6
	v_add_u32_e32 v100, v117, v142
	v_or_b32_e32 v0, 0x800, v0
	s_waitcnt lgkmcnt(0)
	buffer_store_dwordx4 v[150:153], v100, s[0:3], 0 offen sc1
	v_mul_u32_u24_e32 v100, 0xaab, v0
	v_lshrrev_b32_e32 v157, 17, v100
	v_mul_lo_u32 v100, v157, s4
	v_or_b32_e32 v110, s16, v157
	v_add_lshl_u32 v143, v100, v0, 4
	v_mul_lo_u32 v141, v110, s6
	v_mul_u32_u24_e32 v100, 0x310, v157
	v_mul_u32_u24_e32 v110, 0xaab, v144
	v_add3_u32 v100, v100, v143, s14
	v_lshrrev_b32_e32 v158, 17, v110
	ds_read_b128 v[146:149], v100
	v_mul_lo_u32 v110, v158, s4
	v_add_lshl_u32 v144, v110, v144, 4
	v_mul_u32_u24_e32 v110, 0x310, v158
	v_add3_u32 v110, v110, v144, s14
	ds_read_b128 v[150:153], v110
	v_add_u32_e32 v0, v143, v141
	s_waitcnt lgkmcnt(1)
	buffer_store_dwordx4 v[146:149], v0, s[0:3], 0 offen sc1
	v_or_b32_e32 v0, s16, v158
	v_mul_lo_u32 v145, v0, s6
	v_add_u32_e32 v0, v144, v145
	s_waitcnt lgkmcnt(0)
	buffer_store_dwordx4 v[150:153], v0, s[0:3], 0 offen sc1
	v_add_f32_e32 v0, v106, v98
	v_cvt_f16_f32_e32 v0, v0
	v_mov_b32_e32 v106, v107
	v_mov_b32_e32 v107, v108
	v_pk_add_f32 v[106:107], v[106:107], v[128:129]
	v_add_f32_e32 v108, v109, v101
	v_cvt_pk_f16_f32 v107, v106, v107
	v_pack_b32_f16 v106, v0, v107
	v_add_f32_e32 v0, v102, v98
	v_cvt_f16_f32_e32 v0, v0
	v_mov_b32_e32 v102, v103
	v_mov_b32_e32 v103, v104
	v_pk_add_f32 v[102:103], v[102:103], v[128:129]
	v_add_f32_e32 v104, v105, v101
	v_cvt_pk_f16_f32 v103, v102, v103
	v_pack_b32_f16 v102, v0, v103
	v_add_f32_e32 v0, v94, v98
	v_cvt_f16_f32_e32 v0, v0
	v_mov_b32_e32 v94, v95
	v_mov_b32_e32 v95, v96
	v_pk_add_f32 v[94:95], v[94:95], v[128:129]
	v_add_f32_e32 v96, v97, v101
	v_cvt_pk_f16_f32 v95, v94, v95
	v_pack_b32_f16 v94, v0, v95
	v_add_f32_e32 v0, v86, v98
	v_cvt_f16_f32_e32 v0, v0
	v_mov_b32_e32 v86, v87
	v_mov_b32_e32 v87, v88
	v_pk_add_f32 v[86:87], v[86:87], v[128:129]
	v_add_f32_e32 v88, v89, v101
	v_cvt_pk_f16_f32 v87, v86, v87
	v_pack_b32_f16 v86, v0, v87
	v_add_f32_e32 v0, v78, v90
	v_cvt_f16_f32_e32 v0, v0
	v_mov_b32_e32 v78, v79
	v_mov_b32_e32 v79, v80
	v_pk_add_f32 v[78:79], v[78:79], v[126:127]
	v_add_f32_e32 v80, v81, v93
	v_cvt_pk_f16_f32 v79, v78, v79
	v_pack_b32_f16 v78, v0, v79
	v_add_f32_e32 v0, v74, v90
	v_cvt_f16_f32_e32 v0, v0
	v_mov_b32_e32 v74, v75
	v_mov_b32_e32 v75, v76
	v_pk_add_f32 v[74:75], v[74:75], v[126:127]
	v_add_f32_e32 v76, v77, v93
	v_cvt_pk_f16_f32 v75, v74, v75
	v_pack_b32_f16 v74, v0, v75
	v_add_f32_e32 v0, v70, v90
	v_cvt_f16_f32_e32 v0, v0
	v_mov_b32_e32 v70, v71
	v_mov_b32_e32 v71, v72
	v_pk_add_f32 v[70:71], v[70:71], v[126:127]
	v_add_f32_e32 v72, v73, v93
	v_cvt_pk_f16_f32 v71, v70, v71
	v_pack_b32_f16 v70, v0, v71
	v_add_f32_e32 v0, v66, v90
	v_cvt_f16_f32_e32 v0, v0
	v_mov_b32_e32 v66, v67
	v_mov_b32_e32 v67, v68
	v_pk_add_f32 v[66:67], v[66:67], v[126:127]
	v_add_f32_e32 v68, v69, v93
	v_cvt_pk_f16_f32 v67, v66, v67
	v_pack_b32_f16 v66, v0, v67
	v_add_f32_e32 v0, v62, v82
	v_cvt_f16_f32_e32 v0, v0
	v_mov_b32_e32 v62, v63
	v_mov_b32_e32 v63, v64
	v_pk_add_f32 v[62:63], v[62:63], v[124:125]
	v_add_f32_e32 v64, v65, v85
	v_cvt_pk_f16_f32 v63, v62, v63
	v_pack_b32_f16 v62, v0, v63
	v_add_f32_e32 v0, v58, v82
	v_cvt_f16_f32_e32 v0, v0
	v_mov_b32_e32 v58, v59
	v_mov_b32_e32 v59, v60
	v_pk_add_f32 v[58:59], v[58:59], v[124:125]
	v_add_f32_e32 v60, v61, v85
	v_cvt_pk_f16_f32 v59, v58, v59
	v_pack_b32_f16 v58, v0, v59
	v_add_f32_e32 v0, v54, v82
	v_cvt_f16_f32_e32 v0, v0
	v_mov_b32_e32 v54, v55
	v_mov_b32_e32 v55, v56
	v_pk_add_f32 v[54:55], v[54:55], v[124:125]
	v_add_f32_e32 v56, v57, v85
	v_cvt_pk_f16_f32 v55, v54, v55
	v_pack_b32_f16 v54, v0, v55
	v_add_f32_e32 v0, v50, v82
	v_mov_b32_e32 v50, v51
	v_mov_b32_e32 v51, v52
	v_add_f32_e32 v52, v53, v85
	v_cvt_f16_f32_e32 v108, v108
	v_cvt_f16_f32_e32 v104, v104
	v_cvt_f16_f32_e32 v96, v96
	v_cvt_f16_f32_e32 v88, v88
	v_cvt_f16_f32_e32 v80, v80
	v_cvt_f16_f32_e32 v76, v76
	v_cvt_f16_f32_e32 v72, v72
	v_cvt_f16_f32_e32 v68, v68
	v_cvt_f16_f32_e32 v64, v64
	v_cvt_f16_f32_e32 v60, v60
	v_cvt_f16_f32_e32 v56, v56
	v_cvt_f16_f32_e32 v0, v0
	v_cvt_f16_f32_e32 v52, v52
	v_pk_add_f32 v[50:51], v[50:51], v[124:125]
	v_alignbit_b32 v107, v108, v107, 16
	v_cvt_pk_f16_f32 v51, v50, v51
	v_alignbit_b32 v103, v104, v103, 16
	v_alignbit_b32 v95, v96, v95, 16
	v_alignbit_b32 v87, v88, v87, 16
	v_alignbit_b32 v79, v80, v79, 16
	v_alignbit_b32 v75, v76, v75, 16
	v_alignbit_b32 v71, v72, v71, 16
	v_alignbit_b32 v67, v68, v67, 16
	v_alignbit_b32 v63, v64, v63, 16
	v_alignbit_b32 v59, v60, v59, 16
	v_alignbit_b32 v55, v56, v55, 16
	v_pack_b32_f16 v50, v0, v51
	v_alignbit_b32 v51, v52, v51, 16
	s_barrier
	ds_write2_b64 v130, v[106:107], v[78:79] offset1:4
	ds_write2_b64 v132, v[102:103], v[74:75] offset0:32 offset1:36
	ds_write2_b64 v131, v[94:95], v[70:71] offset0:64 offset1:68
	ds_write2_b64 v91, v[86:87], v[66:67] offset0:96 offset1:100
	ds_write_b64 v130, v[62:63] offset:64
	ds_write_b64 v130, v[58:59] offset:12608
	ds_write_b64 v130, v[54:55] offset:25152
	ds_write_b64 v130, v[50:51] offset:37696
	s_waitcnt lgkmcnt(0)
	s_barrier
	global_load_dwordx4 v[50:53], v[122:123], off
	global_load_dwordx4 v[54:57], v[122:123], off offset:1024
	global_load_dwordx4 v[58:61], v[122:123], off offset:2048
	ds_read_b128 v[62:65], v83
	ds_read_b128 v[70:73], v84
	v_mul_lo_u32 v68, v139, s6
	v_add_u32_e32 v0, v68, v111
	ds_read_b128 v[74:77], v99
	s_waitcnt lgkmcnt(2)
	buffer_store_dwordx4 v[62:65], v0, s[0:3], 0 offen sc1
	v_or_b32_e32 v0, s7, v154
	v_mul_lo_u32 v69, v0, s6
	ds_read_b128 v[62:65], v92
	v_add_u32_e32 v0, v113, v69
	s_waitcnt lgkmcnt(2)
	buffer_store_dwordx4 v[70:73], v0, s[0:3], 0 offen sc1
	v_or_b32_e32 v0, s7, v155
	s_nop 0
	v_mul_lo_u32 v72, v0, s6
	v_add_u32_e32 v0, v115, v72
	s_waitcnt lgkmcnt(0)
	buffer_store_dwordx4 v[62:65], v0, s[0:3], 0 offen sc1
	v_or_b32_e32 v0, s7, v156
	v_mul_lo_u32 v70, v0, s6
	ds_read_b128 v[62:65], v100
	v_add_u32_e32 v0, v117, v70
	buffer_store_dwordx4 v[74:77], v0, s[0:3], 0 offen sc1
	v_or_b32_e32 v0, s7, v157
	v_mul_lo_u32 v71, v0, s6
	v_add_u32_e32 v0, v143, v71
	ds_read_b128 v[74:77], v110
	s_waitcnt lgkmcnt(1)
	buffer_store_dwordx4 v[62:65], v0, s[0:3], 0 offen sc1
	ds_read_b128 v[62:65], v134
	ds_read_b128 v[78:81], v134 offset:8192
	ds_read_b128 v[86:89], v134 offset:16384
	ds_read_b128 v[94:97], v134 offset:24576
	ds_read_b128 v[102:105], v134 offset:32768
	ds_read_b128 v[106:109], v134 offset:40960
	ds_read_b128 v[124:127], v134 offset:49152
	ds_read_b128 v[146:149], v134 offset:57344
	v_or_b32_e32 v0, s7, v158
	v_mul_lo_u32 v73, v0, s6
	v_add_u32_e32 v0, v144, v73
	s_waitcnt lgkmcnt(8)
	buffer_store_dwordx4 v[74:77], v0, s[0:3], 0 offen sc1
	s_waitcnt lgkmcnt(7)
	s_nop 0
	v_mfma_f32_16x16x32_f16 v[74:77], v[38:41], v[62:65], 0
	s_waitcnt lgkmcnt(6)
	v_mfma_f32_16x16x32_f16 v[150:153], v[38:41], v[78:81], 0
	s_waitcnt lgkmcnt(5)
	v_mfma_f32_16x16x32_f16 v[154:157], v[38:41], v[86:89], 0
	s_waitcnt lgkmcnt(4)
	v_mfma_f32_16x16x32_f16 v[158:161], v[38:41], v[94:97], 0
	s_waitcnt lgkmcnt(3)
	v_mfma_f32_16x16x32_f16 v[162:165], v[38:41], v[102:105], 0
	s_waitcnt lgkmcnt(2)
	v_mfma_f32_16x16x32_f16 v[166:169], v[38:41], v[106:109], 0
	s_waitcnt lgkmcnt(1)
	v_mfma_f32_16x16x32_f16 v[170:173], v[38:41], v[124:127], 0
	s_waitcnt lgkmcnt(0)
	v_mfma_f32_16x16x32_f16 v[38:41], v[38:41], v[146:149], 0
	v_mfma_f32_16x16x32_f16 v[174:177], v[26:29], v[62:65], 0
	v_mfma_f32_16x16x32_f16 v[178:181], v[26:29], v[78:81], 0
	v_mfma_f32_16x16x32_f16 v[182:185], v[26:29], v[86:89], 0
	v_mfma_f32_16x16x32_f16 v[186:189], v[26:29], v[94:97], 0
	v_mfma_f32_16x16x32_f16 v[190:193], v[26:29], v[102:105], 0
	v_mfma_f32_16x16x32_f16 v[194:197], v[26:29], v[106:109], 0
	v_mfma_f32_16x16x32_f16 v[198:201], v[26:29], v[124:127], 0
	v_mfma_f32_16x16x32_f16 v[26:29], v[26:29], v[146:149], 0
	v_mfma_f32_16x16x32_f16 v[62:65], v[10:13], v[62:65], 0
	v_mfma_f32_16x16x32_f16 v[78:81], v[10:13], v[78:81], 0
	v_mfma_f32_16x16x32_f16 v[86:89], v[10:13], v[86:89], 0
	v_mfma_f32_16x16x32_f16 v[94:97], v[10:13], v[94:97], 0
	v_mfma_f32_16x16x32_f16 v[102:105], v[10:13], v[102:105], 0
	v_mfma_f32_16x16x32_f16 v[106:109], v[10:13], v[106:109], 0
	v_mfma_f32_16x16x32_f16 v[124:127], v[10:13], v[124:127], 0
	v_mfma_f32_16x16x32_f16 v[10:13], v[10:13], v[146:149], 0
	s_mov_b32 s4, 0x34000
	v_add_co_u32_e32 v66, vcc, s4, v118
	s_mov_b32 s4, 0x35000
	s_nop 0
	v_addc_co_u32_e32 v67, vcc, 0, v119, vcc
	v_add_co_u32_e32 v118, vcc, s4, v118
	s_nop 1
	v_addc_co_u32_e32 v119, vcc, 0, v119, vcc
	global_load_dwordx4 v[146:149], v[118:119], off offset:-4096
	global_load_dwordx4 v[202:205], v[122:123], off offset:3072
	global_load_dwordx4 v[206:209], v[66:67], off offset:1024
	ds_read_b128 v[210:213], v1
	ds_read_b128 v[214:217], v1 offset:8192
	ds_read_b128 v[218:221], v1 offset:16384
	ds_read_b128 v[222:225], v1 offset:24576
	ds_read_b128 v[226:229], v1 offset:32768
	ds_read_b128 v[230:233], v1 offset:40960
	ds_read_b128 v[234:237], v1 offset:49152
	ds_read_b128 v[238:241], v1 offset:57344
	s_waitcnt lgkmcnt(7)
	v_mfma_f32_16x16x32_f16 v[74:77], v[22:25], v[210:213], v[74:77]
	s_waitcnt lgkmcnt(6)
	v_mfma_f32_16x16x32_f16 v[150:153], v[22:25], v[214:217], v[150:153]
	s_waitcnt lgkmcnt(5)
	v_mfma_f32_16x16x32_f16 v[154:157], v[22:25], v[218:221], v[154:157]
	s_waitcnt lgkmcnt(4)
	v_mfma_f32_16x16x32_f16 v[158:161], v[22:25], v[222:225], v[158:161]
	s_waitcnt lgkmcnt(3)
	v_mfma_f32_16x16x32_f16 v[162:165], v[22:25], v[226:229], v[162:165]
	s_waitcnt lgkmcnt(2)
	v_mfma_f32_16x16x32_f16 v[166:169], v[22:25], v[230:233], v[166:169]
	s_waitcnt lgkmcnt(1)
	v_mfma_f32_16x16x32_f16 v[170:173], v[22:25], v[234:237], v[170:173]
	s_waitcnt lgkmcnt(0)
	v_mfma_f32_16x16x32_f16 v[22:25], v[22:25], v[238:241], v[38:41]
	v_mfma_f32_16x16x32_f16 v[38:41], v[6:9], v[210:213], v[174:177]
	v_mfma_f32_16x16x32_f16 v[174:177], v[6:9], v[214:217], v[178:181]
	v_mfma_f32_16x16x32_f16 v[178:181], v[6:9], v[218:221], v[182:185]
	v_mfma_f32_16x16x32_f16 v[182:185], v[6:9], v[222:225], v[186:189]
	v_mfma_f32_16x16x32_f16 v[186:189], v[6:9], v[226:229], v[190:193]
	v_mfma_f32_16x16x32_f16 v[190:193], v[6:9], v[230:233], v[194:197]
	v_mfma_f32_16x16x32_f16 v[194:197], v[6:9], v[234:237], v[198:201]
	v_mfma_f32_16x16x32_f16 v[6:9], v[6:9], v[238:241], v[26:29]
	v_mfma_f32_16x16x32_f16 v[26:29], v[2:5], v[210:213], v[62:65]
	v_mfma_f32_16x16x32_f16 v[62:65], v[2:5], v[214:217], v[78:81]
	v_mfma_f32_16x16x32_f16 v[78:81], v[2:5], v[218:221], v[86:89]
	v_mfma_f32_16x16x32_f16 v[86:89], v[2:5], v[222:225], v[94:97]
	v_mfma_f32_16x16x32_f16 v[94:97], v[2:5], v[226:229], v[102:105]
	v_mfma_f32_16x16x32_f16 v[102:105], v[2:5], v[230:233], v[106:109]
	v_mfma_f32_16x16x32_f16 v[106:109], v[2:5], v[234:237], v[124:127]
	v_mfma_f32_16x16x32_f16 v[0:3], v[2:5], v[238:241], v[10:13]
	s_nop 2
	global_load_dwordx4 v[10:13], v[66:67], off offset:2048
	global_load_dwordx4 v[122:125], v[66:67], off offset:3072
	global_load_dwordx4 v[126:129], v[118:119], off
	ds_read_b128 v[198:201], v133
	ds_read_b128 v[210:213], v133 offset:8192
	ds_read_b128 v[214:217], v133 offset:16384
	ds_read_b128 v[218:221], v133 offset:24576
	ds_read_b128 v[222:225], v133 offset:32768
	ds_read_b128 v[226:229], v133 offset:40960
	ds_read_b128 v[230:233], v133 offset:49152
	ds_read_b128 v[234:237], v133 offset:57344
	s_waitcnt lgkmcnt(7)
	v_mfma_f32_16x16x32_f16 v[74:77], v[30:33], v[198:201], v[74:77]
	s_waitcnt lgkmcnt(6)
	v_mfma_f32_16x16x32_f16 v[150:153], v[30:33], v[210:213], v[150:153]
	s_waitcnt lgkmcnt(5)
	v_mfma_f32_16x16x32_f16 v[154:157], v[30:33], v[214:217], v[154:157]
	s_waitcnt lgkmcnt(4)
	v_mfma_f32_16x16x32_f16 v[158:161], v[30:33], v[218:221], v[158:161]
	s_waitcnt lgkmcnt(3)
	v_mfma_f32_16x16x32_f16 v[162:165], v[30:33], v[222:225], v[162:165]
	s_waitcnt lgkmcnt(2)
	v_mfma_f32_16x16x32_f16 v[166:169], v[30:33], v[226:229], v[166:169]
	s_waitcnt lgkmcnt(1)
	v_mfma_f32_16x16x32_f16 v[170:173], v[30:33], v[230:233], v[170:173]
	s_waitcnt lgkmcnt(0)
	v_mfma_f32_16x16x32_f16 v[22:25], v[30:33], v[234:237], v[22:25]
	v_mfma_f32_16x16x32_f16 v[30:33], v[14:17], v[198:201], v[38:41]
	v_mfma_f32_16x16x32_f16 v[38:41], v[14:17], v[210:213], v[174:177]
	v_mfma_f32_16x16x32_f16 v[174:177], v[14:17], v[214:217], v[178:181]
	v_mfma_f32_16x16x32_f16 v[178:181], v[14:17], v[218:221], v[182:185]
	v_mfma_f32_16x16x32_f16 v[182:185], v[14:17], v[222:225], v[186:189]
	v_mfma_f32_16x16x32_f16 v[186:189], v[14:17], v[226:229], v[190:193]
	v_mfma_f32_16x16x32_f16 v[190:193], v[14:17], v[230:233], v[194:197]
	v_mfma_f32_16x16x32_f16 v[4:7], v[14:17], v[234:237], v[6:9]
	v_mfma_f32_16x16x32_f16 v[14:17], v[18:21], v[198:201], v[26:29]
	v_mfma_f32_16x16x32_f16 v[26:29], v[18:21], v[210:213], v[62:65]
	v_mfma_f32_16x16x32_f16 v[62:65], v[18:21], v[214:217], v[78:81]
	v_mfma_f32_16x16x32_f16 v[78:81], v[18:21], v[218:221], v[86:89]
	v_mfma_f32_16x16x32_f16 v[86:89], v[18:21], v[222:225], v[94:97]
	v_mfma_f32_16x16x32_f16 v[94:97], v[18:21], v[226:229], v[102:105]
	v_mfma_f32_16x16x32_f16 v[102:105], v[18:21], v[230:233], v[106:109]
	v_mfma_f32_16x16x32_f16 v[0:3], v[18:21], v[234:237], v[0:3]
	global_load_dwordx4 v[18:21], v[118:119], off offset:1024
	s_nop 0
	global_load_dwordx4 v[106:109], v[118:119], off offset:2048
	global_load_dwordx4 v[194:197], v[118:119], off offset:3072
	ds_read_b128 v[198:201], v135
	ds_read_b128 v[210:213], v135 offset:8192
	ds_read_b128 v[214:217], v135 offset:16384
	ds_read_b128 v[218:221], v135 offset:24576
	ds_read_b128 v[222:225], v135 offset:32768
	ds_read_b128 v[226:229], v135 offset:40960
	ds_read_b128 v[230:233], v135 offset:49152
	ds_read_b128 v[234:237], v135 offset:57344
	s_waitcnt lgkmcnt(7)
	v_mfma_f32_16x16x32_f16 v[74:77], v[46:49], v[198:201], v[74:77]
	s_waitcnt lgkmcnt(6)
	v_mfma_f32_16x16x32_f16 v[150:153], v[46:49], v[210:213], v[150:153]
	s_waitcnt lgkmcnt(5)
	v_mfma_f32_16x16x32_f16 v[154:157], v[46:49], v[214:217], v[154:157]
	s_waitcnt lgkmcnt(4)
	v_mfma_f32_16x16x32_f16 v[158:161], v[46:49], v[218:221], v[158:161]
	s_waitcnt lgkmcnt(3)
	v_mfma_f32_16x16x32_f16 v[162:165], v[46:49], v[222:225], v[162:165]
	s_waitcnt lgkmcnt(2)
	v_mfma_f32_16x16x32_f16 v[166:169], v[46:49], v[226:229], v[166:169]
	s_waitcnt lgkmcnt(1)
	v_mfma_f32_16x16x32_f16 v[170:173], v[46:49], v[230:233], v[170:173]
	s_waitcnt lgkmcnt(0)
	v_mfma_f32_16x16x32_f16 v[22:25], v[46:49], v[234:237], v[22:25]
	v_mfma_f32_16x16x32_f16 v[30:33], v[42:45], v[198:201], v[30:33]
	v_mfma_f32_16x16x32_f16 v[38:41], v[42:45], v[210:213], v[38:41]
	v_mfma_f32_16x16x32_f16 v[46:49], v[42:45], v[214:217], v[174:177]
	v_mfma_f32_16x16x32_f16 v[174:177], v[42:45], v[218:221], v[178:181]
	v_mfma_f32_16x16x32_f16 v[178:181], v[42:45], v[222:225], v[182:185]
	v_mfma_f32_16x16x32_f16 v[182:185], v[42:45], v[226:229], v[186:189]
	v_mfma_f32_16x16x32_f16 v[186:189], v[42:45], v[230:233], v[190:193]
	v_mfma_f32_16x16x32_f16 v[4:7], v[42:45], v[234:237], v[4:7]
	v_mfma_f32_16x16x32_f16 v[14:17], v[34:37], v[198:201], v[14:17]
	v_mfma_f32_16x16x32_f16 v[26:29], v[34:37], v[210:213], v[26:29]
	v_mfma_f32_16x16x32_f16 v[42:45], v[34:37], v[214:217], v[62:65]
	v_mfma_f32_16x16x32_f16 v[62:65], v[34:37], v[218:221], v[78:81]
	v_mfma_f32_16x16x32_f16 v[78:81], v[34:37], v[222:225], v[86:89]
	v_mfma_f32_16x16x32_f16 v[86:89], v[34:37], v[226:229], v[94:97]
	v_mfma_f32_16x16x32_f16 v[94:97], v[34:37], v[230:233], v[102:105]
	v_mfma_f32_16x16x32_f16 v[0:3], v[34:37], v[234:237], v[0:3]
	ds_read_b128 v[34:37], v136
	s_nop 0
	ds_read_b128 v[102:105], v136 offset:8192
	ds_read_b128 v[190:193], v136 offset:16384
	ds_read_b128 v[198:201], v136 offset:24576
	ds_read_b128 v[210:213], v136 offset:32768
	ds_read_b128 v[214:217], v136 offset:40960
	ds_read_b128 v[218:221], v136 offset:49152
	ds_read_b128 v[222:225], v136 offset:57344
	s_waitcnt vmcnt(17) lgkmcnt(7)
	v_mfma_f32_16x16x32_f16 v[74:77], v[50:53], v[34:37], v[74:77]
	s_waitcnt lgkmcnt(6)
	v_mfma_f32_16x16x32_f16 v[150:153], v[50:53], v[102:105], v[150:153]
	s_waitcnt lgkmcnt(5)
	v_mfma_f32_16x16x32_f16 v[154:157], v[50:53], v[190:193], v[154:157]
	s_waitcnt lgkmcnt(4)
	v_mfma_f32_16x16x32_f16 v[158:161], v[50:53], v[198:201], v[158:161]
	s_waitcnt lgkmcnt(3)
	v_mfma_f32_16x16x32_f16 v[162:165], v[50:53], v[210:213], v[162:165]
	s_waitcnt lgkmcnt(2)
	v_mfma_f32_16x16x32_f16 v[166:169], v[50:53], v[214:217], v[166:169]
	s_waitcnt lgkmcnt(1)
	v_mfma_f32_16x16x32_f16 v[170:173], v[50:53], v[218:221], v[170:173]
	s_waitcnt lgkmcnt(0)
	v_mfma_f32_16x16x32_f16 v[22:25], v[50:53], v[222:225], v[22:25]
	s_waitcnt vmcnt(16)
	v_mfma_f32_16x16x32_f16 v[30:33], v[54:57], v[34:37], v[30:33]
	v_mfma_f32_16x16x32_f16 v[38:41], v[54:57], v[102:105], v[38:41]
	v_mfma_f32_16x16x32_f16 v[46:49], v[54:57], v[190:193], v[46:49]
	v_mfma_f32_16x16x32_f16 v[50:53], v[54:57], v[198:201], v[174:177]
	v_mfma_f32_16x16x32_f16 v[174:177], v[54:57], v[210:213], v[178:181]
	v_mfma_f32_16x16x32_f16 v[178:181], v[54:57], v[214:217], v[182:185]
	v_mfma_f32_16x16x32_f16 v[182:185], v[54:57], v[218:221], v[186:189]
	v_mfma_f32_16x16x32_f16 v[4:7], v[54:57], v[222:225], v[4:7]
	s_waitcnt vmcnt(15)
	v_mfma_f32_16x16x32_f16 v[14:17], v[58:61], v[34:37], v[14:17]
	v_mfma_f32_16x16x32_f16 v[26:29], v[58:61], v[102:105], v[26:29]
	v_mfma_f32_16x16x32_f16 v[34:37], v[58:61], v[190:193], v[42:45]
	v_mfma_f32_16x16x32_f16 v[42:45], v[58:61], v[198:201], v[62:65]
	v_mfma_f32_16x16x32_f16 v[54:57], v[58:61], v[210:213], v[78:81]
	v_mfma_f32_16x16x32_f16 v[62:65], v[58:61], v[214:217], v[86:89]
	v_mfma_f32_16x16x32_f16 v[78:81], v[58:61], v[218:221], v[94:97]
	v_mfma_f32_16x16x32_f16 v[0:3], v[58:61], v[222:225], v[0:3]
	ds_read_b128 v[58:61], v137
	ds_read_b128 v[86:89], v137 offset:8192
	ds_read_b128 v[94:97], v137 offset:16384
	ds_read_b128 v[102:105], v137 offset:24576
	ds_read_b128 v[186:189], v137 offset:32768
	ds_read_b128 v[190:193], v137 offset:40960
	ds_read_b128 v[198:201], v137 offset:49152
	ds_read_b128 v[134:137], v137 offset:57344
	s_waitcnt vmcnt(7) lgkmcnt(7)
	v_mfma_f32_16x16x32_f16 v[74:77], v[202:205], v[58:61], v[74:77]
	s_waitcnt lgkmcnt(6)
	v_mfma_f32_16x16x32_f16 v[150:153], v[202:205], v[86:89], v[150:153]
	s_waitcnt lgkmcnt(5)
	v_mfma_f32_16x16x32_f16 v[154:157], v[202:205], v[94:97], v[154:157]
	s_waitcnt lgkmcnt(4)
	v_mfma_f32_16x16x32_f16 v[158:161], v[202:205], v[102:105], v[158:161]
	s_waitcnt lgkmcnt(3)
	v_mfma_f32_16x16x32_f16 v[162:165], v[202:205], v[186:189], v[162:165]
	s_waitcnt lgkmcnt(2)
	v_mfma_f32_16x16x32_f16 v[166:169], v[202:205], v[190:193], v[166:169]
	s_waitcnt lgkmcnt(1)
	v_mfma_f32_16x16x32_f16 v[170:173], v[202:205], v[198:201], v[170:173]
	s_waitcnt lgkmcnt(0)
	v_mfma_f32_16x16x32_f16 v[22:25], v[202:205], v[134:137], v[22:25]
	v_mfma_f32_16x16x32_f16 v[30:33], v[146:149], v[58:61], v[30:33]
	v_mfma_f32_16x16x32_f16 v[38:41], v[146:149], v[86:89], v[38:41]
	v_mfma_f32_16x16x32_f16 v[46:49], v[146:149], v[94:97], v[46:49]
	v_mfma_f32_16x16x32_f16 v[50:53], v[146:149], v[102:105], v[50:53]
	v_mfma_f32_16x16x32_f16 v[174:177], v[146:149], v[186:189], v[174:177]
	v_mfma_f32_16x16x32_f16 v[178:181], v[146:149], v[190:193], v[178:181]
	v_mfma_f32_16x16x32_f16 v[182:185], v[146:149], v[198:201], v[182:185]
	v_mfma_f32_16x16x32_f16 v[4:7], v[146:149], v[134:137], v[4:7]
	s_waitcnt vmcnt(6)
	v_mfma_f32_16x16x32_f16 v[14:17], v[206:209], v[58:61], v[14:17]
	v_mfma_f32_16x16x32_f16 v[26:29], v[206:209], v[86:89], v[26:29]
	v_mfma_f32_16x16x32_f16 v[34:37], v[206:209], v[94:97], v[34:37]
	v_mfma_f32_16x16x32_f16 v[42:45], v[206:209], v[102:105], v[42:45]
	v_mfma_f32_16x16x32_f16 v[54:57], v[206:209], v[186:189], v[54:57]
	v_mfma_f32_16x16x32_f16 v[58:61], v[206:209], v[190:193], v[62:65]
	v_mfma_f32_16x16x32_f16 v[62:65], v[206:209], v[198:201], v[78:81]
	v_mfma_f32_16x16x32_f16 v[0:3], v[206:209], v[134:137], v[0:3]
	s_nop 1
	ds_read_b128 v[78:81], v138
	ds_read_b128 v[86:89], v138 offset:8192
	ds_read_b128 v[94:97], v138 offset:16384
	ds_read_b128 v[102:105], v138 offset:24576
	ds_read_b128 v[134:137], v138 offset:32768
	ds_read_b128 v[146:149], v138 offset:40960
	ds_read_b128 v[186:189], v138 offset:49152
	ds_read_b128 v[190:193], v138 offset:57344
	s_waitcnt vmcnt(5) lgkmcnt(7)
	v_mfma_f32_16x16x32_f16 v[74:77], v[10:13], v[78:81], v[74:77]
	s_waitcnt lgkmcnt(6)
	v_mfma_f32_16x16x32_f16 v[150:153], v[10:13], v[86:89], v[150:153]
	s_waitcnt lgkmcnt(5)
	v_mfma_f32_16x16x32_f16 v[154:157], v[10:13], v[94:97], v[154:157]
	s_waitcnt lgkmcnt(4)
	v_mfma_f32_16x16x32_f16 v[158:161], v[10:13], v[102:105], v[158:161]
	s_waitcnt lgkmcnt(3)
	v_mfma_f32_16x16x32_f16 v[162:165], v[10:13], v[134:137], v[162:165]
	s_waitcnt lgkmcnt(2)
	v_mfma_f32_16x16x32_f16 v[166:169], v[10:13], v[146:149], v[166:169]
	s_waitcnt lgkmcnt(1)
	v_mfma_f32_16x16x32_f16 v[170:173], v[10:13], v[186:189], v[170:173]
	s_waitcnt lgkmcnt(0)
	v_mfma_f32_16x16x32_f16 v[8:11], v[10:13], v[190:193], v[22:25]
	s_waitcnt vmcnt(4)
	v_mfma_f32_16x16x32_f16 v[22:25], v[122:125], v[78:81], v[30:33]
	v_mfma_f32_16x16x32_f16 v[30:33], v[122:125], v[86:89], v[38:41]
	v_mfma_f32_16x16x32_f16 v[198:201], v[122:125], v[94:97], v[46:49]
	v_mfma_f32_16x16x32_f16 v[48:51], v[122:125], v[102:105], v[50:53]
	v_mfma_f32_16x16x32_f16 v[174:177], v[122:125], v[134:137], v[174:177]
	v_mfma_f32_16x16x32_f16 v[178:181], v[122:125], v[146:149], v[178:181]
	v_mfma_f32_16x16x32_f16 v[182:185], v[122:125], v[186:189], v[182:185]
	v_mfma_f32_16x16x32_f16 v[4:7], v[122:125], v[190:193], v[4:7]
	s_waitcnt vmcnt(3)
	v_mfma_f32_16x16x32_f16 v[12:15], v[126:129], v[78:81], v[14:17]
	v_mfma_f32_16x16x32_f16 v[78:81], v[126:129], v[86:89], v[26:29]
	v_mfma_f32_16x16x32_f16 v[86:89], v[126:129], v[94:97], v[34:37]
	v_mfma_f32_16x16x32_f16 v[40:43], v[126:129], v[102:105], v[42:45]
	v_mfma_f32_16x16x32_f16 v[94:97], v[126:129], v[134:137], v[54:57]
	v_mfma_f32_16x16x32_f16 v[102:105], v[126:129], v[146:149], v[58:61]
	v_mfma_f32_16x16x32_f16 v[64:67], v[126:129], v[186:189], v[62:65]
	v_mfma_f32_16x16x32_f16 v[0:3], v[126:129], v[190:193], v[0:3]
	s_nop 1
	ds_read_b128 v[60:63], v140
	ds_read_b128 v[122:125], v140 offset:8192
	ds_read_b128 v[126:129], v140 offset:16384
	ds_read_b128 v[134:137], v140 offset:24576
	ds_read_b128 v[146:149], v140 offset:32768
	ds_read_b128 v[186:189], v140 offset:40960
	ds_read_b128 v[190:193], v140 offset:49152
	ds_read_b128 v[202:205], v140 offset:57344
	s_waitcnt vmcnt(2) lgkmcnt(7)
	v_mfma_f32_16x16x32_f16 v[74:77], v[18:21], v[60:63], v[74:77]
	s_waitcnt lgkmcnt(6)
	v_mfma_f32_16x16x32_f16 v[150:153], v[18:21], v[122:125], v[150:153]
	s_waitcnt lgkmcnt(5)
	v_mfma_f32_16x16x32_f16 v[154:157], v[18:21], v[126:129], v[154:157]
	s_waitcnt lgkmcnt(4)
	v_mfma_f32_16x16x32_f16 v[158:161], v[18:21], v[134:137], v[158:161]
	s_waitcnt lgkmcnt(3)
	v_mfma_f32_16x16x32_f16 v[56:59], v[18:21], v[146:149], v[162:165]
	s_waitcnt lgkmcnt(2)
	v_mfma_f32_16x16x32_f16 v[52:55], v[18:21], v[186:189], v[166:169]
	s_waitcnt lgkmcnt(1)
	v_mfma_f32_16x16x32_f16 v[44:47], v[18:21], v[190:193], v[170:173]
	s_waitcnt lgkmcnt(0)
	v_mfma_f32_16x16x32_f16 v[36:39], v[18:21], v[202:205], v[8:11]
	s_waitcnt vmcnt(1)
	v_mfma_f32_16x16x32_f16 v[162:165], v[106:109], v[60:63], v[22:25]
	v_mfma_f32_16x16x32_f16 v[166:169], v[106:109], v[122:125], v[30:33]
	v_mfma_f32_16x16x32_f16 v[170:173], v[106:109], v[126:129], v[198:201]
	v_mfma_f32_16x16x32_f16 v[198:201], v[106:109], v[134:137], v[48:51]
	v_mfma_f32_16x16x32_f16 v[32:35], v[106:109], v[146:149], v[174:177]
	v_mfma_f32_16x16x32_f16 v[24:27], v[106:109], v[186:189], v[178:181]
	v_mfma_f32_16x16x32_f16 v[20:23], v[106:109], v[190:193], v[182:185]
	v_mfma_f32_16x16x32_f16 v[16:19], v[106:109], v[202:205], v[4:7]
	s_waitcnt vmcnt(0)
	v_mfma_f32_16x16x32_f16 v[106:109], v[194:197], v[60:63], v[12:15]
	v_mfma_f32_16x16x32_f16 v[78:81], v[194:197], v[122:125], v[78:81]
	v_mfma_f32_16x16x32_f16 v[86:89], v[194:197], v[126:129], v[86:89]
	v_mfma_f32_16x16x32_f16 v[60:63], v[194:197], v[134:137], v[40:43]
	v_mfma_f32_16x16x32_f16 v[12:15], v[194:197], v[146:149], v[94:97]
	v_mfma_f32_16x16x32_f16 v[8:11], v[194:197], v[186:189], v[102:105]
	v_mfma_f32_16x16x32_f16 v[4:7], v[194:197], v[190:193], v[64:67]
	v_mfma_f32_16x16x32_f16 v[0:3], v[194:197], v[202:205], v[0:3]
	global_load_dwordx4 v[48:51], v[120:121], off offset:1536
	global_load_dwordx4 v[40:43], v[120:121], off offset:1600
	global_load_dwordx4 v[28:31], v[120:121], off offset:1664
	v_mov_b32_e32 v94, v155
	v_mov_b32_e32 v95, v156
	v_mov_b32_e32 v96, v159
	v_mov_b32_e32 v97, v160
	v_mov_b32_e32 v64, v151
	v_mov_b32_e32 v65, v152
	v_mov_b32_e32 v102, v167
	v_mov_b32_e32 v103, v168
	v_mov_b32_e32 v104, v171
	v_mov_b32_e32 v105, v172
	v_mov_b32_e32 v118, v199
	v_mov_b32_e32 v119, v200
	s_barrier
	s_waitcnt vmcnt(2)
	v_pk_add_f32 v[74:75], v[74:75], v[48:49]
	v_add_f32_e32 v82, v150, v48
	v_pk_mov_b32 v[120:121], v[48:49], v[50:51] op_sel:[1,0]
	v_add_f32_e32 v49, v153, v51
	s_waitcnt vmcnt(1)
	v_pk_add_f32 v[122:123], v[162:163], v[40:41]
	v_add_f32_e32 v98, v166, v40
	v_pk_mov_b32 v[66:67], v[40:41], v[42:43] op_sel:[1,0]
	v_add_f32_e32 v41, v169, v43
	v_pk_add_f32 v[76:77], v[76:77], v[50:51]
	v_add_f32_e32 v50, v154, v48
	v_add_f32_e32 v85, v157, v51
	v_add_f32_e32 v90, v158, v48
	v_add_f32_e32 v93, v161, v51
	v_pk_add_f32 v[124:125], v[164:165], v[42:43]
	v_add_f32_e32 v42, v170, v40
	v_add_f32_e32 v101, v173, v43
	v_add_f32_e32 v126, v198, v40
	v_add_f32_e32 v127, v201, v43
	v_cvt_f16_f32_e32 v82, v82
	v_cvt_f16_f32_e32 v49, v49
	v_cvt_f16_f32_e32 v98, v98
	v_cvt_f16_f32_e32 v41, v41
	v_cvt_pk_f16_f32 v74, v74, v75
	v_cvt_pk_f16_f32 v75, v76, v77
	v_cvt_f16_f32_e32 v50, v50
	v_pk_add_f32 v[76:77], v[94:95], v[120:121]
	v_cvt_f16_f32_e32 v85, v85
	v_cvt_f16_f32_e32 v90, v90
	v_pk_add_f32 v[94:95], v[96:97], v[120:121]
	v_cvt_f16_f32_e32 v93, v93
	v_cvt_pk_f16_f32 v96, v122, v123
	v_cvt_f16_f32_e32 v42, v42
	v_cvt_f16_f32_e32 v101, v101
	v_cvt_f16_f32_e32 v122, v126
	v_cvt_f16_f32_e32 v123, v127
	v_pk_add_f32 v[64:65], v[64:65], v[120:121]
	v_pk_add_f32 v[102:103], v[102:103], v[66:67]
	v_pk_add_f32 v[104:105], v[104:105], v[66:67]
	v_pk_add_f32 v[118:119], v[118:119], v[66:67]
	v_cvt_pk_f16_f32 v65, v64, v65
	v_cvt_pk_f16_f32 v76, v76, v77
	v_cvt_pk_f16_f32 v77, v94, v95
	v_cvt_pk_f16_f32 v95, v102, v103
	s_waitcnt vmcnt(0)
	v_pk_add_f32 v[106:107], v[106:107], v[28:29]
	v_pk_add_f32 v[108:109], v[108:109], v[30:31]
	v_cvt_pk_f16_f32 v97, v124, v125
	v_cvt_pk_f16_f32 v102, v104, v105
	v_cvt_pk_f16_f32 v103, v118, v119
	v_pack_b32_f16 v64, v82, v65
	v_alignbit_b32 v65, v49, v65, 16
	v_pack_b32_f16 v94, v98, v95
	v_alignbit_b32 v95, v41, v95, 16
	v_add_f32_e32 v78, v78, v28
	v_cvt_pk_f16_f32 v106, v106, v107
	v_cvt_pk_f16_f32 v107, v108, v109
	ds_write2_b64 v130, v[74:75], v[96:97] offset1:4
	ds_write_b64 v130, v[106:107] offset:64
	v_pack_b32_f16 v74, v50, v76
	v_alignbit_b32 v75, v85, v76, 16
	v_pack_b32_f16 v76, v90, v77
	v_alignbit_b32 v77, v93, v77, 16
	v_pack_b32_f16 v96, v42, v102
	v_alignbit_b32 v97, v101, v102, 16
	v_pack_b32_f16 v102, v122, v103
	v_alignbit_b32 v103, v123, v103, 16
	ds_write2_b64 v132, v[64:65], v[94:95] offset0:32 offset1:36
	ds_write2_b64 v131, v[74:75], v[96:97] offset0:64 offset1:68
	ds_write2_b64 v91, v[76:77], v[102:103] offset0:96 offset1:100
	v_pk_mov_b32 v[64:65], v[28:29], v[30:31] op_sel:[1,0]
	v_add_f32_e32 v29, v81, v31
	v_cvt_f16_f32_e32 v78, v78
	v_cvt_f16_f32_e32 v29, v29
	v_mov_b32_e32 v74, v79
	v_mov_b32_e32 v75, v80
	v_pk_add_f32 v[74:75], v[74:75], v[64:65]
	v_add_f32_e32 v56, v56, v48
	v_cvt_pk_f16_f32 v30, v74, v75
	v_pack_b32_f16 v74, v78, v30
	v_alignbit_b32 v75, v29, v30, 16
	v_add_f32_e32 v29, v86, v28
	v_add_f32_e32 v30, v89, v31
	v_cvt_f16_f32_e32 v29, v29
	v_cvt_f16_f32_e32 v30, v30
	ds_write_b64 v130, v[74:75] offset:12608
	v_mov_b32_e32 v74, v87
	v_mov_b32_e32 v75, v88
	v_pk_add_f32 v[74:75], v[74:75], v[64:65]
	v_add_f32_e32 v52, v52, v48
	v_cvt_pk_f16_f32 v41, v74, v75
	v_pack_b32_f16 v74, v29, v41
	v_alignbit_b32 v75, v30, v41, 16
	v_add_f32_e32 v29, v60, v28
	v_add_f32_e32 v30, v63, v31
	v_cvt_f16_f32_e32 v29, v29
	v_cvt_f16_f32_e32 v30, v30
	v_mov_b32_e32 v60, v61
	v_mov_b32_e32 v61, v62
	v_pk_add_f32 v[60:61], v[60:61], v[64:65]
	ds_write_b64 v130, v[74:75] offset:25152
	v_cvt_pk_f16_f32 v41, v60, v61
	v_pack_b32_f16 v60, v29, v41
	v_alignbit_b32 v61, v30, v41, 16
	ds_write_b64 v130, v[60:61] offset:37696
	s_waitcnt lgkmcnt(0)
	s_barrier
	ds_read_b128 v[60:63], v83
	ds_read_b128 v[74:77], v84
	v_add_u32_e32 v29, 0x300, v111
	v_add_u32_e32 v30, v29, v112
	v_add_f32_e32 v44, v44, v48
	s_waitcnt lgkmcnt(1)
	buffer_store_dwordx4 v[60:63], v30, s[0:3], 0 offen sc1
	v_add_u32_e32 v30, 0x300, v113
	ds_read_b128 v[60:63], v92
	v_add_u32_e32 v41, v30, v114
	s_waitcnt lgkmcnt(1)
	buffer_store_dwordx4 v[74:77], v41, s[0:3], 0 offen sc1
	ds_read_b128 v[74:77], v99
	v_add_u32_e32 v41, 0x300, v115
	v_add_u32_e32 v42, v41, v116
	s_waitcnt lgkmcnt(1)
	buffer_store_dwordx4 v[60:63], v42, s[0:3], 0 offen sc1
	v_add_u32_e32 v42, 0x300, v117
	ds_read_b128 v[60:63], v100
	v_add_u32_e32 v49, v42, v142
	s_waitcnt lgkmcnt(1)
	buffer_store_dwordx4 v[74:77], v49, s[0:3], 0 offen sc1
	ds_read_b128 v[74:77], v110
	v_add_u32_e32 v49, 0x300, v143
	v_add_u32_e32 v50, v49, v141
	s_waitcnt lgkmcnt(1)
	buffer_store_dwordx4 v[60:63], v50, s[0:3], 0 offen sc1
	v_add_u32_e32 v50, 0x300, v144
	v_add_f32_e32 v36, v36, v48
	v_add_u32_e32 v60, v50, v145
	s_waitcnt lgkmcnt(0)
	buffer_store_dwordx4 v[74:77], v60, s[0:3], 0 offen sc1
	v_cvt_f16_f32_e32 v60, v56
	v_mov_b32_e32 v56, v57
	v_mov_b32_e32 v57, v58
	v_add_f32_e32 v58, v59, v51
	v_cvt_f16_f32_e32 v58, v58
	v_pk_add_f32 v[56:57], v[56:57], v[120:121]
	v_add_f32_e32 v32, v32, v40
	v_cvt_pk_f16_f32 v57, v56, v57
	v_pack_b32_f16 v56, v60, v57
	v_alignbit_b32 v57, v58, v57, 16
	v_cvt_f16_f32_e32 v58, v52
	v_mov_b32_e32 v52, v53
	v_mov_b32_e32 v53, v54
	v_add_f32_e32 v54, v55, v51
	v_cvt_f16_f32_e32 v54, v54
	v_pk_add_f32 v[52:53], v[52:53], v[120:121]
	v_add_f32_e32 v24, v24, v40
	v_cvt_pk_f16_f32 v53, v52, v53
	v_pack_b32_f16 v52, v58, v53
	v_alignbit_b32 v53, v54, v53, 16
	v_cvt_f16_f32_e32 v54, v44
	v_mov_b32_e32 v44, v45
	v_mov_b32_e32 v45, v46
	v_add_f32_e32 v46, v47, v51
	v_cvt_f16_f32_e32 v46, v46
	v_pk_add_f32 v[44:45], v[44:45], v[120:121]
	s_nop 0
	v_cvt_pk_f16_f32 v45, v44, v45
	v_pack_b32_f16 v44, v54, v45
	v_alignbit_b32 v45, v46, v45, 16
	v_cvt_f16_f32_e32 v46, v36
	v_mov_b32_e32 v36, v37
	v_mov_b32_e32 v37, v38
	v_add_f32_e32 v38, v39, v51
	v_cvt_f16_f32_e32 v38, v38
	v_pk_add_f32 v[36:37], v[36:37], v[120:121]
	s_barrier
	v_cvt_pk_f16_f32 v37, v36, v37
	v_pack_b32_f16 v36, v46, v37
	v_alignbit_b32 v37, v38, v37, 16
	v_cvt_f16_f32_e32 v38, v32
	v_mov_b32_e32 v32, v33
	v_mov_b32_e32 v33, v34
	v_add_f32_e32 v34, v35, v43
	v_cvt_f16_f32_e32 v34, v34
	v_pk_add_f32 v[32:33], v[32:33], v[66:67]
	s_nop 0
	v_cvt_pk_f16_f32 v33, v32, v33
	v_pack_b32_f16 v32, v38, v33
	v_alignbit_b32 v33, v34, v33, 16
	ds_write2_b64 v130, v[56:57], v[32:33] offset1:4
	v_cvt_f16_f32_e32 v32, v24
	v_mov_b32_e32 v24, v25
	v_mov_b32_e32 v25, v26
	v_add_f32_e32 v26, v27, v43
	v_cvt_f16_f32_e32 v26, v26
	v_pk_add_f32 v[24:25], v[24:25], v[66:67]
	v_add_f32_e32 v20, v20, v40
	v_cvt_pk_f16_f32 v25, v24, v25
	v_pack_b32_f16 v24, v32, v25
	v_alignbit_b32 v25, v26, v25, 16
	ds_write2_b64 v132, v[52:53], v[24:25] offset0:32 offset1:36
	v_cvt_f16_f32_e32 v24, v20
	v_mov_b32_e32 v20, v21
	v_mov_b32_e32 v21, v22
	v_add_f32_e32 v22, v23, v43
	v_cvt_f16_f32_e32 v22, v22
	v_pk_add_f32 v[20:21], v[20:21], v[66:67]
	v_add_f32_e32 v16, v16, v40
	v_cvt_pk_f16_f32 v21, v20, v21
	v_pack_b32_f16 v20, v24, v21
	v_alignbit_b32 v21, v22, v21, 16
	ds_write2_b64 v131, v[44:45], v[20:21] offset0:64 offset1:68
	v_cvt_f16_f32_e32 v20, v16
	v_mov_b32_e32 v16, v17
	v_mov_b32_e32 v17, v18
	v_add_f32_e32 v18, v19, v43
	v_cvt_f16_f32_e32 v18, v18
	v_pk_add_f32 v[16:17], v[16:17], v[66:67]
	v_add_f32_e32 v12, v12, v28
	v_cvt_pk_f16_f32 v17, v16, v17
	v_pack_b32_f16 v16, v20, v17
	v_alignbit_b32 v17, v18, v17, 16
	ds_write2_b64 v91, v[36:37], v[16:17] offset0:96 offset1:100
	v_cvt_f16_f32_e32 v16, v12
	v_mov_b32_e32 v12, v13
	v_mov_b32_e32 v13, v14
	v_add_f32_e32 v14, v15, v31
	v_cvt_f16_f32_e32 v14, v14
	v_pk_add_f32 v[12:13], v[12:13], v[64:65]
	v_add_f32_e32 v8, v8, v28
	v_cvt_pk_f16_f32 v13, v12, v13
	v_pack_b32_f16 v12, v16, v13
	v_alignbit_b32 v13, v14, v13, 16
	ds_write_b64 v130, v[12:13] offset:64
	v_cvt_f16_f32_e32 v12, v8
	v_mov_b32_e32 v8, v9
	v_mov_b32_e32 v9, v10
	v_add_f32_e32 v10, v11, v31
	v_cvt_f16_f32_e32 v10, v10
	v_pk_add_f32 v[8:9], v[8:9], v[64:65]
	v_add_f32_e32 v4, v4, v28
	v_cvt_pk_f16_f32 v9, v8, v9
	v_pack_b32_f16 v8, v12, v9
	v_alignbit_b32 v9, v10, v9, 16
	ds_write_b64 v130, v[8:9] offset:12608
	v_cvt_f16_f32_e32 v8, v4
	v_mov_b32_e32 v4, v5
	v_mov_b32_e32 v5, v6
	v_add_f32_e32 v6, v7, v31
	v_cvt_f16_f32_e32 v6, v6
	v_pk_add_f32 v[4:5], v[4:5], v[64:65]
	v_add_f32_e32 v0, v0, v28
	v_cvt_pk_f16_f32 v5, v4, v5
	v_pack_b32_f16 v4, v8, v5
	v_alignbit_b32 v5, v6, v5, 16
	ds_write_b64 v130, v[4:5] offset:25152
	v_cvt_f16_f32_e32 v4, v0
	v_mov_b32_e32 v0, v1
	v_mov_b32_e32 v1, v2
	v_add_f32_e32 v2, v3, v31
	v_cvt_f16_f32_e32 v2, v2
	v_pk_add_f32 v[0:1], v[0:1], v[64:65]
	v_add_u32_e32 v8, v29, v68
	v_cvt_pk_f16_f32 v1, v0, v1
	v_pack_b32_f16 v0, v4, v1
	v_alignbit_b32 v1, v2, v1, 16
	ds_write_b64 v130, v[0:1] offset:37696
	s_waitcnt lgkmcnt(0)
	s_barrier
	ds_read_b128 v[0:3], v83
	ds_read_b128 v[4:7], v84
	v_add_u32_e32 v12, v42, v70
	s_waitcnt lgkmcnt(1)
	buffer_store_dwordx4 v[0:3], v8, s[0:3], 0 offen sc1
	ds_read_b128 v[0:3], v92
	v_add_u32_e32 v8, v30, v69
	s_waitcnt lgkmcnt(1)
	buffer_store_dwordx4 v[4:7], v8, s[0:3], 0 offen sc1
	v_add_u32_e32 v8, v41, v72
	ds_read_b128 v[4:7], v99
	s_waitcnt lgkmcnt(1)
	buffer_store_dwordx4 v[0:3], v8, s[0:3], 0 offen sc1
	ds_read_b128 v[0:3], v100
	ds_read_b128 v[8:11], v110
	s_waitcnt lgkmcnt(2)
	buffer_store_dwordx4 v[4:7], v12, s[0:3], 0 offen sc1
	s_nop 1
	v_add_u32_e32 v4, v49, v71
	s_waitcnt lgkmcnt(1)
	buffer_store_dwordx4 v[0:3], v4, s[0:3], 0 offen sc1
	s_nop 1
	v_add_u32_e32 v0, v50, v73
	s_waitcnt lgkmcnt(0)
	buffer_store_dwordx4 v[8:11], v0, s[0:3], 0 offen sc1
	s_endpgm

amdhsa.kernels:
  - .agpr_count:     0
    .args:
      - .actual_access:  read_only
        .address_space:  global
        .offset:         0
        .size:           8
        .value_kind:     global_buffer
      - .actual_access:  read_only
        .address_space:  global
        .offset:         8
        .size:           8
        .value_kind:     global_buffer
      - .actual_access:  read_only
        .address_space:  global
        .offset:         16
        .size:           8
        .value_kind:     global_buffer
      - .actual_access:  read_only
        .address_space:  global
        .offset:         24
        .size:           8
        .value_kind:     global_buffer
      - .actual_access:  read_only
        .address_space:  global
        .offset:         32
        .size:           8
        .value_kind:     global_buffer
      - .actual_access:  read_only
        .address_space:  global
        .offset:         40
        .size:           8
        .value_kind:     global_buffer
      - .actual_access:  read_only
        .address_space:  global
        .offset:         48
        .size:           8
        .value_kind:     global_buffer
      - .actual_access:  read_only
        .address_space:  global
        .offset:         56
        .size:           8
        .value_kind:     global_buffer
      - .actual_access:  write_only
        .address_space:  global
        .offset:         64
        .size:           8
        .value_kind:     global_buffer
      - .actual_access:  write_only
        .address_space:  global
        .offset:         72
        .size:           8
        .value_kind:     global_buffer
      - .actual_access:  write_only
        .address_space:  global
        .offset:         80
        .size:           8
        .value_kind:     global_buffer
      - .actual_access:  write_only
        .address_space:  global
        .offset:         88
        .size:           8
        .value_kind:     global_buffer
    .group_segment_fixed_size: 0
    .kernarg_segment_align: 8
    .kernarg_segment_size: 96
    .language:       OpenCL C
    .language_version:
      - 2
      - 0
    .max_flat_workgroup_size: 256
    .name:           _Z8k_prep_wPKfS0_S0_S0_S0_S0_S0_S0_PDF16_PfS1_S1_
    .private_segment_fixed_size: 0
    .sgpr_count:     23
    .sgpr_spill_count: 0
    .symbol:         _Z8k_prep_wPKfS0_S0_S0_S0_S0_S0_S0_PDF16_PfS1_S1_.kd
    .uniform_work_group_size: 1
    .uses_dynamic_stack: false
    .vgpr_count:     15
    .vgpr_spill_count: 0
    .wavefront_size: 64
  - .agpr_count:     0
    .args:
      - .actual_access:  read_only
        .address_space:  global
        .offset:         0
        .size:           8
        .value_kind:     global_buffer
      - .actual_access:  read_only
        .address_space:  global
        .offset:         8
        .size:           8
        .value_kind:     global_buffer
      - .actual_access:  read_only
        .address_space:  global
        .offset:         16
        .size:           8
        .value_kind:     global_buffer
      - .actual_access:  read_only
        .address_space:  global
        .offset:         24
        .size:           8
        .value_kind:     global_buffer
      - .actual_access:  write_only
        .address_space:  global
        .offset:         32
        .size:           8
        .value_kind:     global_buffer
      - .actual_access:  read_only
        .address_space:  global
        .offset:         40
        .size:           8
        .value_kind:     global_buffer
      - .actual_access:  read_only
        .address_space:  global
        .offset:         48
        .size:           8
        .value_kind:     global_buffer
      - .actual_access:  write_only
        .address_space:  global
        .offset:         56
        .size:           8
        .value_kind:     global_buffer
      - .offset:         64
        .size:           4
        .value_kind:     by_value
      - .offset:         68
        .size:           4
        .value_kind:     by_value
    .group_segment_fixed_size: 115712
    .kernarg_segment_align: 8
    .kernarg_segment_size: 72
    .language:       OpenCL C
    .language_version:
      - 2
      - 0
    .max_flat_workgroup_size: 512
    .name:           _Z8k_stageAPKfS0_S0_S0_PDF16_PKDF16_S0_S1_ii
    .private_segment_fixed_size: 0
    .sgpr_count:     28
    .sgpr_spill_count: 0
    .symbol:         _Z8k_stageAPKfS0_S0_S0_PDF16_PKDF16_S0_S1_ii.kd
    .uniform_work_group_size: 1
    .uses_dynamic_stack: false
    .vgpr_count:     256
    .vgpr_spill_count: 0
    .wavefront_size: 64
  - .agpr_count:     112
    .args:
      - .actual_access:  read_only
        .address_space:  global
        .offset:         0
        .size:           8
        .value_kind:     global_buffer
      - .actual_access:  read_only
        .address_space:  global
        .offset:         8
        .size:           8
        .value_kind:     global_buffer
      - .actual_access:  read_only
        .address_space:  global
        .offset:         16
        .size:           8
        .value_kind:     global_buffer
      - .actual_access:  read_only
        .address_space:  global
        .offset:         24
        .size:           8
        .value_kind:     global_buffer
      - .actual_access:  read_only
        .address_space:  global
        .offset:         32
        .size:           8
        .value_kind:     global_buffer
      - .actual_access:  write_only
        .address_space:  global
        .offset:         40
        .size:           8
        .value_kind:     global_buffer
    .group_segment_fixed_size: 107712
    .kernarg_segment_align: 8
    .kernarg_segment_size: 48
    .language:       OpenCL C
    .language_version:
      - 2
      - 0
    .max_flat_workgroup_size: 256
    .name:           _Z7k_conv4PKDF16_S0_S0_PKfS2_Pf
    .private_segment_fixed_size: 0
    .sgpr_count:     36
    .sgpr_spill_count: 0
    .symbol:         _Z7k_conv4PKDF16_S0_S0_PKfS2_Pf.kd
    .uniform_work_group_size: 1
    .uses_dynamic_stack: false
    .vgpr_count:     336
    .vgpr_spill_count: 0
    .wavefront_size: 64
  - .agpr_count:     0
    .args:
      - .offset:         0
        .size:           112
        .value_kind:     by_value
      - .actual_access:  read_only
        .address_space:  global
        .offset:         112
        .size:           8
        .value_kind:     global_buffer
      - .actual_access:  read_only
        .address_space:  global
        .offset:         120
        .size:           8
        .value_kind:     global_buffer
      - .actual_access:  write_only
        .address_space:  global
        .offset:         128
        .size:           8
        .value_kind:     global_buffer
      - .offset:         136
        .size:           4
        .value_kind:     by_value
      - .offset:         140
        .size:           4
        .value_kind:     by_value
      - .offset:         144
        .size:           4
        .value_kind:     by_value
    .group_segment_fixed_size: 115712
    .kernarg_segment_align: 8
    .kernarg_segment_size: 148
    .language:       OpenCL C
    .language_version:
      - 2
      - 0
    .max_flat_workgroup_size: 512
    .name:           _Z7k_stageILi0ELi8EEv8AttnArgsPKDF16_PKfPDF16_iii
    .private_segment_fixed_size: 0
    .sgpr_count:     41
    .sgpr_spill_count: 0
    .symbol:         _Z7k_stageILi0ELi8EEv8AttnArgsPKDF16_PKfPDF16_iii.kd
    .uniform_work_group_size: 1
    .uses_dynamic_stack: false
    .vgpr_count:     255
    .vgpr_spill_count: 0
    .wavefront_size: 64
  - .agpr_count:     0
    .args:
      - .offset:         0
        .size:           112
        .value_kind:     by_value
      - .actual_access:  read_only
        .address_space:  global
        .offset:         112
        .size:           8
        .value_kind:     global_buffer
      - .actual_access:  read_only
        .address_space:  global
        .offset:         120
        .size:           8
        .value_kind:     global_buffer
      - .actual_access:  write_only
        .address_space:  global
        .offset:         128
        .size:           8
        .value_kind:     global_buffer
      - .offset:         136
        .size:           4
        .value_kind:     by_value
      - .offset:         140
        .size:           4
        .value_kind:     by_value
      - .offset:         144
        .size:           4
        .value_kind:     by_value
    .group_segment_fixed_size: 82944
    .kernarg_segment_align: 8
    .kernarg_segment_size: 148
    .language:       OpenCL C
    .language_version:
      - 2
      - 0
    .max_flat_workgroup_size: 512
    .name:           _Z7k_stageILi1ELi4EEv8AttnArgsPKDF16_PKfPDF16_iii
    .private_segment_fixed_size: 0
    .sgpr_count:     55
    .sgpr_spill_count: 0
    .symbol:         _Z7k_stageILi1ELi4EEv8AttnArgsPKDF16_PKfPDF16_iii.kd
    .uniform_work_group_size: 1
    .uses_dynamic_stack: false
    .vgpr_count:     252
    .vgpr_spill_count: 0
    .wavefront_size: 64
  - .agpr_count:     0
    .args:
      - .offset:         0
        .size:           112
        .value_kind:     by_value
      - .actual_access:  read_only
        .address_space:  global
        .offset:         112
        .size:           8
        .value_kind:     global_buffer
      - .actual_access:  read_only
        .address_space:  global
        .offset:         120
        .size:           8
        .value_kind:     global_buffer
      - .actual_access:  write_only
        .address_space:  global
        .offset:         128
        .size:           8
        .value_kind:     global_buffer
      - .offset:         136
        .size:           4
        .value_kind:     by_value
      - .offset:         140
        .size:           4
        .value_kind:     by_value
      - .offset:         144
        .size:           4
        .value_kind:     by_value
    .group_segment_fixed_size: 82944
    .kernarg_segment_align: 8
    .kernarg_segment_size: 148
    .language:       OpenCL C
    .language_version:
      - 2
      - 0
    .max_flat_workgroup_size: 512
    .name:           _Z7k_stageILi0ELi4EEv8AttnArgsPKDF16_PKfPDF16_iii
    .private_segment_fixed_size: 0
    .sgpr_count:     38
    .sgpr_spill_count: 0
    .symbol:         _Z7k_stageILi0ELi4EEv8AttnArgsPKDF16_PKfPDF16_iii.kd
    .uniform_work_group_size: 1
    .uses_dynamic_stack: false
    .vgpr_count:     246
    .vgpr_spill_count: 0
    .wavefront_size: 64
  - .agpr_count:     0
    .args:
      - .offset:         0
        .size:           112
        .value_kind:     by_value
    .group_segment_fixed_size: 0
    .kernarg_segment_align: 8
    .kernarg_segment_size: 112
    .language:       OpenCL C
    .language_version:
      - 2
      - 0
    .max_flat_workgroup_size: 512
    .name:           _Z7k_attn2ILi2EEv8AttnArgs
    .private_segment_fixed_size: 0
    .sgpr_count:     102
    .sgpr_spill_count: 0
    .symbol:         _Z7k_attn2ILi2EEv8AttnArgs.kd
    .uniform_work_group_size: 1
    .uses_dynamic_stack: false
    .vgpr_count:     252
    .vgpr_spill_count: 0
    .wavefront_size: 64
